# v16 + nt on cold once-read PROJ loads only: P5 retention-unit reads + gate_a, P6 gate_b
# baseline (speedup 1.0000x reference)
.LBB0_1066:
	v_lshl_or_b32 v6, s61, 8, v204
	v_add_u32_e32 v8, s60, v202
	v_ashrrev_i32_e32 v7, 31, v6
	v_mov_b64_e32 v[10:11], s[18:19]
	v_mad_i64_i32 v[2:3], s[0:1], v8, s56, v[10:11]
	v_lshlrev_b64 v[12:13], 1, v[6:7]
	v_lshl_add_u32 v251, v8, 11, v6
	v_mad_u32_u24 v250, v8, s56, v12
	global_load_dwordx4 v[214:217], v250, s[18:19] nt
	global_load_dwordx2 v[238:239], v251, s[16:17]
	v_lshl_add_u32 v251, v8, 11, v6
	v_mad_u32_u24 v250, v8, s56, v12
	global_load_dwordx4 v[218:221], v250, s[18:19] offset:256 nt
	global_load_dwordx2 v[240:241], v251, s[16:17] offset:128
	v_add_u32_e32 v250, 16, v8
	v_lshl_add_u32 v251, v250, 11, v6
	v_mad_u32_u24 v250, v250, s56, v12
	global_load_dwordx4 v[222:225], v250, s[18:19] nt
	global_load_dwordx2 v[242:243], v251, s[16:17]
	v_add_u32_e32 v250, 16, v8
	v_lshl_add_u32 v251, v250, 11, v6
	v_mad_u32_u24 v250, v250, s56, v12
	global_load_dwordx4 v[226:229], v250, s[18:19] offset:256 nt
	global_load_dwordx2 v[244:245], v251, s[16:17] offset:128
	v_add_u32_e32 v250, 32, v8
	v_lshl_add_u32 v251, v250, 11, v6
	v_mad_u32_u24 v250, v250, s56, v12
	global_load_dwordx4 v[230:233], v250, s[18:19] nt
	global_load_dwordx2 v[246:247], v251, s[16:17]
	v_add_u32_e32 v250, 32, v8
	v_lshl_add_u32 v251, v250, 11, v6
	v_mad_u32_u24 v250, v250, s56, v12
	global_load_dwordx4 v[234:237], v250, s[18:19] offset:256 nt
	global_load_dwordx2 v[248:249], v251, s[16:17] offset:128
	s_nop 15
	s_nop 15
	s_nop 15
	v_lshl_add_u64 v[14:15], v[2:3], 0, v[12:13]
	v_ashrrev_i32_e32 v9, 31, v8
	v_lshlrev_b64 v[16:17], 11, v[8:9]
	v_lshl_add_u64 v[18:19], s[16:17], 0, v[16:17]
	v_lshl_add_u64 v[18:19], v[18:19], 0, v[6:7]
	v_pk_mul_f32 v[22:23], v[154:155], s[28:29] op_sel_hi:[1,0]
	v_pk_mul_f32 v[20:21], v[156:157], s[28:29] op_sel_hi:[1,0]
	v_pk_mul_f32 v[26:27], v[158:159], s[28:29] op_sel_hi:[1,0]
	v_pk_mul_f32 v[24:25], v[160:161], s[28:29] op_sel_hi:[1,0]
	s_waitcnt vmcnt(11)
	v_mov_b64_e32 v[2:3], v[214:215]
	v_mov_b64_e32 v[4:5], v[216:217]
	s_waitcnt vmcnt(10)
	v_mov_b64_e32 v[28:29], v[238:239]
	v_add_u32_e32 v250, 48, v8
	v_lshl_add_u32 v251, v250, 11, v6
	v_mad_u32_u24 v250, v250, s56, v12
	global_load_dwordx4 v[214:217], v250, s[18:19] nt
	global_load_dwordx2 v[238:239], v251, s[16:17]
	v_lshlrev_b32_e32 v9, 16, v2
	v_and_b32_e32 v2, 0xffff0000, v2
	v_mul_f32_e32 v9, 0xbfb8aa3b, v9
	v_lshlrev_b32_e32 v30, 16, v3
	v_mul_f32_e32 v2, 0xbfb8aa3b, v2
	v_exp_f32_e32 v9, v9
	v_and_b32_e32 v3, 0xffff0000, v3
	v_mul_f32_e32 v30, 0xbfb8aa3b, v30
	v_exp_f32_e32 v2, v2
	v_mul_f32_e32 v3, 0xbfb8aa3b, v3
	v_exp_f32_e32 v30, v30
	v_exp_f32_e32 v3, v3
	v_add_f32_e32 v9, 1.0, v9
	v_add_f32_e32 v2, 1.0, v2
	v_add_f32_e32 v30, 1.0, v30
	v_lshlrev_b32_e32 v31, 16, v4
	v_add_f32_e32 v3, 1.0, v3
	v_mul_f32_e32 v31, 0xbfb8aa3b, v31
	v_exp_f32_e32 v31, v31
	s_nop 0
	v_add_f32_e32 v31, 1.0, v31
	v_and_b32_e32 v4, 0xffff0000, v4
	v_mul_f32_e32 v4, 0xbfb8aa3b, v4
	v_exp_f32_e32 v4, v4
	v_rcp_f32_e32 v179, v9
	v_rcp_f32_e32 v9, v2
	v_rcp_f32_e32 v154, v30
	v_rcp_f32_e32 v155, v3
	v_add_f32_e32 v3, 1.0, v4
	v_lshlrev_b32_e32 v32, 16, v5
	v_rcp_f32_e32 v156, v31
	v_mul_f32_e32 v32, 0xbfb8aa3b, v32
	v_exp_f32_e32 v32, v32
	s_nop 0
	v_add_f32_e32 v4, 1.0, v32
	v_and_b32_e32 v5, 0xffff0000, v5
	v_mul_f32_e32 v5, 0xbfb8aa3b, v5
	v_exp_f32_e32 v5, v5
	v_rcp_f32_e32 v157, v3
	v_add_f32_e32 v5, 1.0, v5
	v_rcp_f32_e32 v158, v4
	v_rcp_f32_e32 v159, v5
	v_cvt_pk_f32_fp8_e32 v[2:3], v28
	v_cvt_pk_f32_fp8_sdwa v[4:5], v28 src0_sel:WORD_1
	v_mov_b32_e32 v33, v26
	v_cvt_pk_f32_fp8_e32 v[30:31], v29
	v_mov_b32_e32 v32, v2
	v_pk_mul_f32 v[32:33], v[32:33], v[178:179]
	v_mov_b32_e32 v26, v3
	v_mov_b32_e32 v179, v9
	v_pk_mul_f32 v[2:3], v[26:27], v[178:179]
	v_mov_b32_e32 v179, v154
	v_add_f32_e32 v9, v2, v3
	v_mov_b32_e32 v2, v4
	v_mov_b32_e32 v3, v24
	v_pk_mul_f32 v[2:3], v[2:3], v[178:179]
	v_mov_b32_e32 v24, v5
	v_mov_b32_e32 v179, v155
	v_cvt_pk_f32_fp8_sdwa v[28:29], v29 src0_sel:WORD_1
	v_add_f32_e32 v4, v2, v3
	v_pk_mul_f32 v[2:3], v[24:25], v[178:179]
	v_mov_b32_e32 v179, v156
	v_add_f32_e32 v5, v2, v3
	v_mov_b32_e32 v2, v30
	v_mov_b32_e32 v3, v22
	v_pk_mul_f32 v[2:3], v[2:3], v[178:179]
	v_mov_b32_e32 v22, v31
	v_mov_b32_e32 v179, v157
	v_add_f32_e32 v24, v2, v3
	v_pk_mul_f32 v[2:3], v[22:23], v[178:179]
	v_mov_b32_e32 v179, v158
	v_add_f32_e32 v22, v2, v3
	v_mov_b32_e32 v2, v28
	v_mov_b32_e32 v3, v20
	v_pk_mul_f32 v[2:3], v[2:3], v[178:179]
	v_mov_b32_e32 v20, v29
	v_mov_b32_e32 v179, v159
	v_add_f32_e32 v32, v32, v33
	v_add_f32_e32 v23, v2, v3
	v_pk_mul_f32 v[2:3], v[20:21], v[178:179]
	v_mul_f32_e32 v4, 0x41800000, v4
	v_add_f32_e32 v20, v2, v3
	v_mul_f32_e32 v2, 0x41800000, v32
	v_mul_f32_e32 v3, 0x41800000, v9
	v_med3_f32 v9, v2, s57, v207
	v_med3_f32 v3, v3, s57, v207
	v_mov_b32_e32 v2, v167
	v_cvt_pk_fp8_f32 v2, v9, v3
	v_mul_f32_e32 v3, 0x41800000, v5
	v_med3_f32 v4, v4, s57, v207
	v_med3_f32 v3, v3, s57, v207
	v_cvt_pk_fp8_f32 v2, v4, v3 op_sel:[0,0,1]
	v_mul_f32_e32 v3, 0x41800000, v24
	v_mul_f32_e32 v4, 0x41800000, v22
	v_med3_f32 v9, v3, s57, v207
	v_med3_f32 v4, v4, s57, v207
	v_mov_b32_e32 v3, v167
	v_cvt_pk_fp8_f32 v3, v9, v4
	v_mul_f32_e32 v5, 0x41800000, v23
	v_mul_f32_e32 v4, 0x41800000, v20
	v_med3_f32 v5, v5, s57, v207
	v_med3_f32 v4, v4, s57, v207
	v_cvt_pk_fp8_f32 v3, v5, v4 op_sel:[0,0,1]
	v_lshl_add_u64 v[4:5], s[20:21], 0, v[16:17]
	v_lshl_add_u64 v[16:17], v[4:5], 0, v[6:7]
	v_pk_mul_f32 v[24:25], v[146:147], s[28:29] op_sel_hi:[1,0]
	global_store_dwordx2 v[16:17], v[2:3], off
	s_nop 0
	v_pk_mul_f32 v[20:21], v[150:151], s[28:29] op_sel_hi:[1,0]
	v_pk_mul_f32 v[18:19], v[152:153], s[28:29] op_sel_hi:[1,0]
	v_pk_mul_f32 v[22:23], v[148:149], s[28:29] op_sel_hi:[1,0]
	s_waitcnt vmcnt(11)
	v_mov_b64_e32 v[2:3], v[218:219]
	v_mov_b64_e32 v[4:5], v[220:221]
	v_lshlrev_b32_e32 v9, 16, v2
	v_mul_f32_e32 v9, 0xbfb8aa3b, v9
	v_exp_f32_e32 v9, v9
	v_and_b32_e32 v2, 0xffff0000, v2
	v_mul_f32_e32 v2, 0xbfb8aa3b, v2
	v_exp_f32_e32 v2, v2
	v_add_f32_e32 v9, 1.0, v9
	v_add_f32_e32 v2, 1.0, v2
	v_lshlrev_b32_e32 v27, 16, v3
	v_mul_f32_e32 v27, 0xbfb8aa3b, v27
	v_rcp_f32_e32 v179, v9
	v_exp_f32_e32 v27, v27
	s_nop 0
	v_add_f32_e32 v27, 1.0, v27
	v_and_b32_e32 v3, 0xffff0000, v3
	v_mul_f32_e32 v3, 0xbfb8aa3b, v3
	v_rcp_f32_e32 v9, v2
	v_exp_f32_e32 v3, v3
	s_nop 0
	v_add_f32_e32 v3, 1.0, v3
	v_rcp_f32_e32 v31, v27
	v_lshlrev_b32_e32 v27, 16, v4
	v_mul_f32_e32 v27, 0xbfb8aa3b, v27
	v_exp_f32_e32 v27, v27
	s_nop 0
	v_add_f32_e32 v27, 1.0, v27
	v_and_b32_e32 v4, 0xffff0000, v4
	v_mul_f32_e32 v4, 0xbfb8aa3b, v4
	v_exp_f32_e32 v4, v4
	v_rcp_f32_e32 v30, v3
	v_add_f32_e32 v4, 1.0, v4
	v_rcp_f32_e32 v32, v27
	v_lshlrev_b32_e32 v27, 16, v5
	v_mul_f32_e32 v27, 0xbfb8aa3b, v27
	v_exp_f32_e32 v27, v27
	s_nop 0
	v_add_f32_e32 v26, 1.0, v27
	v_rcp_f32_e32 v33, v4
	v_and_b32_e32 v4, 0xffff0000, v5
	v_mul_f32_e32 v4, 0xbfb8aa3b, v4
	v_exp_f32_e32 v4, v4
	s_nop 0
	v_add_f32_e32 v4, 1.0, v4
	v_rcp_f32_e32 v146, v26
	v_mov_b32_e32 v29, v20
	v_rcp_f32_e32 v147, v4
	s_waitcnt vmcnt(10)
	v_mov_b64_e32 v[14:15], v[240:241]
	v_add_u32_e32 v250, 48, v8
	v_lshl_add_u32 v251, v250, 11, v6
	v_mad_u32_u24 v250, v250, s56, v12
	global_load_dwordx4 v[218:221], v250, s[18:19] offset:256 nt
	global_load_dwordx2 v[240:241], v251, s[16:17] offset:128
	v_cvt_pk_f32_fp8_e32 v[2:3], v14
	v_cvt_pk_f32_fp8_sdwa v[4:5], v14 src0_sel:WORD_1
	v_cvt_pk_f32_fp8_e32 v[26:27], v15
	v_cvt_pk_f32_fp8_sdwa v[14:15], v15 src0_sel:WORD_1
	v_mov_b32_e32 v28, v2
	v_pk_mul_f32 v[28:29], v[28:29], v[178:179]
	v_mov_b32_e32 v20, v3
	v_mov_b32_e32 v179, v9
	v_pk_mul_f32 v[2:3], v[20:21], v[178:179]
	v_mov_b32_e32 v179, v31
	v_add_f32_e32 v9, v2, v3
	v_mov_b32_e32 v2, v4
	v_mov_b32_e32 v3, v18
	v_pk_mul_f32 v[2:3], v[2:3], v[178:179]
	v_mov_b32_e32 v18, v5
	v_mov_b32_e32 v179, v30
	v_add_f32_e32 v4, v2, v3
	v_pk_mul_f32 v[2:3], v[18:19], v[178:179]
	v_mov_b32_e32 v179, v32
	v_add_f32_e32 v5, v2, v3
	v_mov_b32_e32 v2, v26
	v_mov_b32_e32 v3, v24
	v_pk_mul_f32 v[2:3], v[2:3], v[178:179]
	v_mov_b32_e32 v24, v27
	v_mov_b32_e32 v179, v33
	v_add_f32_e32 v18, v2, v3
	v_pk_mul_f32 v[2:3], v[24:25], v[178:179]
	v_mov_b32_e32 v179, v146
	v_add_f32_e32 v19, v2, v3
	v_mov_b32_e32 v2, v14
	v_mov_b32_e32 v3, v22
	v_pk_mul_f32 v[2:3], v[2:3], v[178:179]
	v_mov_b32_e32 v22, v15
	v_mov_b32_e32 v179, v147
	v_add_f32_e32 v28, v28, v29
	v_add_f32_e32 v14, v2, v3
	v_pk_mul_f32 v[2:3], v[22:23], v[178:179]
	v_mul_f32_e32 v4, 0x41800000, v4
	v_add_f32_e32 v15, v2, v3
	v_mul_f32_e32 v2, 0x41800000, v28
	v_mul_f32_e32 v3, 0x41800000, v9
	v_med3_f32 v9, v2, s57, v207
	v_med3_f32 v3, v3, s57, v207
	v_mov_b32_e32 v2, v167
	v_cvt_pk_fp8_f32 v2, v9, v3
	v_mul_f32_e32 v3, 0x41800000, v5
	v_med3_f32 v4, v4, s57, v207
	v_med3_f32 v3, v3, s57, v207
	v_cvt_pk_fp8_f32 v2, v4, v3 op_sel:[0,0,1]
	v_mul_f32_e32 v3, 0x41800000, v18
	v_mul_f32_e32 v4, 0x41800000, v19
	v_med3_f32 v9, v3, s57, v207
	v_med3_f32 v4, v4, s57, v207
	v_mov_b32_e32 v3, v167
	v_cvt_pk_fp8_f32 v3, v9, v4
	v_mul_f32_e32 v5, 0x41800000, v14
	v_mul_f32_e32 v4, 0x41800000, v15
	v_med3_f32 v5, v5, s57, v207
	v_med3_f32 v4, v4, s57, v207
	v_cvt_pk_fp8_f32 v3, v5, v4 op_sel:[0,0,1]
	v_pk_mul_f32 v[28:29], v[138:139], s[28:29] op_sel_hi:[1,0]
	v_pk_mul_f32 v[26:27], v[140:141], s[28:29] op_sel_hi:[1,0]
	v_pk_mul_f32 v[24:25], v[142:143], s[28:29] op_sel_hi:[1,0]
	global_store_dwordx2 v[16:17], v[2:3], off offset:128
	v_add_u32_e32 v16, 16, v8
	v_mad_i64_i32 v[2:3], s[0:1], v16, s56, v[10:11]
	v_lshl_add_u64 v[14:15], v[2:3], 0, v[12:13]
	v_ashrrev_i32_e32 v17, 31, v16
	v_lshlrev_b64 v[18:19], 11, v[16:17]
	v_lshl_add_u64 v[16:17], s[16:17], 0, v[18:19]
	v_lshl_add_u64 v[16:17], v[16:17], 0, v[6:7]
	v_pk_mul_f32 v[22:23], v[144:145], s[28:29] op_sel_hi:[1,0]
	s_waitcnt vmcnt(11)
	v_mov_b64_e32 v[2:3], v[222:223]
	v_mov_b64_e32 v[4:5], v[224:225]
	v_lshlrev_b32_e32 v9, 16, v2
	v_mul_f32_e32 v9, 0xbfb8aa3b, v9
	v_exp_f32_e32 v9, v9
	v_and_b32_e32 v2, 0xffff0000, v2
	v_mul_f32_e32 v2, 0xbfb8aa3b, v2
	v_exp_f32_e32 v2, v2
	v_add_f32_e32 v9, 1.0, v9
	v_add_f32_e32 v2, 1.0, v2
	v_lshlrev_b32_e32 v31, 16, v3
	v_mul_f32_e32 v31, 0xbfb8aa3b, v31
	v_rcp_f32_e32 v179, v9
	v_exp_f32_e32 v31, v31
	s_nop 0
	v_add_f32_e32 v31, 1.0, v31
	v_and_b32_e32 v3, 0xffff0000, v3
	v_mul_f32_e32 v3, 0xbfb8aa3b, v3
	v_rcp_f32_e32 v9, v2
	v_exp_f32_e32 v3, v3
	s_nop 0
	v_add_f32_e32 v3, 1.0, v3
	v_rcp_f32_e32 v139, v31
	v_lshlrev_b32_e32 v31, 16, v4
	v_mul_f32_e32 v31, 0xbfb8aa3b, v31
	v_exp_f32_e32 v31, v31
	s_nop 0
	v_add_f32_e32 v31, 1.0, v31
	v_and_b32_e32 v4, 0xffff0000, v4
	v_mul_f32_e32 v4, 0xbfb8aa3b, v4
	v_exp_f32_e32 v4, v4
	v_rcp_f32_e32 v138, v3
	v_add_f32_e32 v4, 1.0, v4
	v_rcp_f32_e32 v140, v31
	v_lshlrev_b32_e32 v31, 16, v5
	v_mul_f32_e32 v31, 0xbfb8aa3b, v31
	v_exp_f32_e32 v31, v31
	s_nop 0
	v_add_f32_e32 v30, 1.0, v31
	v_rcp_f32_e32 v141, v4
	v_and_b32_e32 v4, 0xffff0000, v5
	v_mul_f32_e32 v4, 0xbfb8aa3b, v4
	v_exp_f32_e32 v4, v4
	s_nop 0
	v_add_f32_e32 v4, 1.0, v4
	v_rcp_f32_e32 v142, v30
	v_mov_b32_e32 v33, v24
	v_rcp_f32_e32 v143, v4
	s_waitcnt vmcnt(10)
	v_mov_b64_e32 v[20:21], v[242:243]
	v_add_u32_e32 v250, 128, v8
	v_lshl_add_u32 v251, v250, 11, v6
	v_mad_u32_u24 v250, v250, s56, v12
	global_load_dwordx4 v[222:225], v250, s[18:19] nt
	global_load_dwordx2 v[242:243], v251, s[16:17]
	v_cvt_pk_f32_fp8_e32 v[2:3], v20
	v_cvt_pk_f32_fp8_sdwa v[4:5], v20 src0_sel:WORD_1
	v_cvt_pk_f32_fp8_e32 v[30:31], v21
	v_cvt_pk_f32_fp8_sdwa v[20:21], v21 src0_sel:WORD_1
	v_mov_b32_e32 v32, v2
	v_pk_mul_f32 v[32:33], v[32:33], v[178:179]
	v_mov_b32_e32 v24, v3
	v_mov_b32_e32 v179, v9
	v_pk_mul_f32 v[2:3], v[24:25], v[178:179]
	v_mov_b32_e32 v179, v139
	v_add_f32_e32 v9, v2, v3
	v_mov_b32_e32 v2, v4
	v_mov_b32_e32 v3, v22
	v_pk_mul_f32 v[2:3], v[2:3], v[178:179]
	v_mov_b32_e32 v22, v5
	v_mov_b32_e32 v179, v138
	v_add_f32_e32 v4, v2, v3
	v_pk_mul_f32 v[2:3], v[22:23], v[178:179]
	v_mov_b32_e32 v179, v140
	v_add_f32_e32 v5, v2, v3
	v_mov_b32_e32 v2, v30
	v_mov_b32_e32 v3, v28
	v_pk_mul_f32 v[2:3], v[2:3], v[178:179]
	v_mov_b32_e32 v28, v31
	v_mov_b32_e32 v179, v141
	v_add_f32_e32 v22, v2, v3
	v_pk_mul_f32 v[2:3], v[28:29], v[178:179]
	v_mov_b32_e32 v179, v142
	v_add_f32_e32 v23, v2, v3
	v_mov_b32_e32 v2, v20
	v_mov_b32_e32 v3, v26
	v_pk_mul_f32 v[2:3], v[2:3], v[178:179]
	v_mov_b32_e32 v26, v21
	v_mov_b32_e32 v179, v143
	v_add_f32_e32 v32, v32, v33
	v_add_f32_e32 v20, v2, v3
	v_pk_mul_f32 v[2:3], v[26:27], v[178:179]
	v_mul_f32_e32 v4, 0x41800000, v4
	v_add_f32_e32 v21, v2, v3
	v_mul_f32_e32 v2, 0x41800000, v32
	v_mul_f32_e32 v3, 0x41800000, v9
	v_med3_f32 v9, v2, s57, v207
	v_med3_f32 v3, v3, s57, v207
	v_mov_b32_e32 v2, v167
	v_cvt_pk_fp8_f32 v2, v9, v3
	v_mul_f32_e32 v3, 0x41800000, v5
	v_med3_f32 v4, v4, s57, v207
	v_med3_f32 v3, v3, s57, v207
	v_cvt_pk_fp8_f32 v2, v4, v3 op_sel:[0,0,1]
	v_mul_f32_e32 v3, 0x41800000, v22
	v_mul_f32_e32 v4, 0x41800000, v23
	v_med3_f32 v9, v3, s57, v207
	v_med3_f32 v4, v4, s57, v207
	v_mov_b32_e32 v3, v167
	v_cvt_pk_fp8_f32 v3, v9, v4
	v_mul_f32_e32 v5, 0x41800000, v20
	v_mul_f32_e32 v4, 0x41800000, v21
	v_med3_f32 v5, v5, s57, v207
	v_med3_f32 v4, v4, s57, v207
	v_cvt_pk_fp8_f32 v3, v5, v4 op_sel:[0,0,1]
	v_lshl_add_u64 v[4:5], s[20:21], 0, v[18:19]
	v_lshl_add_u64 v[18:19], v[4:5], 0, v[6:7]
	v_pk_mul_f32 v[24:25], v[130:131], s[28:29] op_sel_hi:[1,0]
	global_store_dwordx2 v[18:19], v[2:3], off
	s_nop 0
	v_pk_mul_f32 v[20:21], v[134:135], s[28:29] op_sel_hi:[1,0]
	v_pk_mul_f32 v[16:17], v[136:137], s[28:29] op_sel_hi:[1,0]
	v_pk_mul_f32 v[22:23], v[132:133], s[28:29] op_sel_hi:[1,0]
	s_waitcnt vmcnt(11)
	v_mov_b64_e32 v[2:3], v[226:227]
	v_mov_b64_e32 v[4:5], v[228:229]
	v_lshlrev_b32_e32 v9, 16, v2
	v_mul_f32_e32 v9, 0xbfb8aa3b, v9
	v_exp_f32_e32 v9, v9
	v_and_b32_e32 v2, 0xffff0000, v2
	v_mul_f32_e32 v2, 0xbfb8aa3b, v2
	v_exp_f32_e32 v2, v2
	v_add_f32_e32 v9, 1.0, v9
	v_add_f32_e32 v2, 1.0, v2
	v_lshlrev_b32_e32 v27, 16, v3
	v_mul_f32_e32 v27, 0xbfb8aa3b, v27
	v_rcp_f32_e32 v179, v9
	v_exp_f32_e32 v27, v27
	s_nop 0
	v_add_f32_e32 v27, 1.0, v27
	v_and_b32_e32 v3, 0xffff0000, v3
	v_mul_f32_e32 v3, 0xbfb8aa3b, v3
	v_rcp_f32_e32 v9, v2
	v_exp_f32_e32 v3, v3
	s_nop 0
	v_add_f32_e32 v3, 1.0, v3
	v_rcp_f32_e32 v31, v27
	v_lshlrev_b32_e32 v27, 16, v4
	v_mul_f32_e32 v27, 0xbfb8aa3b, v27
	v_exp_f32_e32 v27, v27
	s_nop 0
	v_add_f32_e32 v27, 1.0, v27
	v_and_b32_e32 v4, 0xffff0000, v4
	v_mul_f32_e32 v4, 0xbfb8aa3b, v4
	v_exp_f32_e32 v4, v4
	v_rcp_f32_e32 v30, v3
	v_add_f32_e32 v4, 1.0, v4
	v_rcp_f32_e32 v32, v27
	v_lshlrev_b32_e32 v27, 16, v5
	v_mul_f32_e32 v27, 0xbfb8aa3b, v27
	v_exp_f32_e32 v27, v27
	s_nop 0
	v_add_f32_e32 v26, 1.0, v27
	v_rcp_f32_e32 v33, v4
	v_and_b32_e32 v4, 0xffff0000, v5
	v_mul_f32_e32 v4, 0xbfb8aa3b, v4
	v_exp_f32_e32 v4, v4
	s_nop 0
	v_add_f32_e32 v4, 1.0, v4
	v_rcp_f32_e32 v130, v26
	v_mov_b32_e32 v29, v20
	v_rcp_f32_e32 v131, v4
	s_waitcnt vmcnt(10)
	v_mov_b64_e32 v[14:15], v[244:245]
	v_add_u32_e32 v250, 128, v8
	v_lshl_add_u32 v251, v250, 11, v6
	v_mad_u32_u24 v250, v250, s56, v12
	global_load_dwordx4 v[226:229], v250, s[18:19] offset:256 nt
	global_load_dwordx2 v[244:245], v251, s[16:17] offset:128
	v_cvt_pk_f32_fp8_e32 v[2:3], v14
	v_cvt_pk_f32_fp8_sdwa v[4:5], v14 src0_sel:WORD_1
	v_cvt_pk_f32_fp8_e32 v[26:27], v15
	v_cvt_pk_f32_fp8_sdwa v[14:15], v15 src0_sel:WORD_1
	v_mov_b32_e32 v28, v2
	v_pk_mul_f32 v[28:29], v[28:29], v[178:179]
	v_mov_b32_e32 v20, v3
	v_mov_b32_e32 v179, v9
	v_pk_mul_f32 v[2:3], v[20:21], v[178:179]
	v_mov_b32_e32 v179, v31
	v_add_f32_e32 v9, v2, v3
	v_mov_b32_e32 v2, v4
	v_mov_b32_e32 v3, v16
	v_pk_mul_f32 v[2:3], v[2:3], v[178:179]
	v_mov_b32_e32 v16, v5
	v_mov_b32_e32 v179, v30
	v_add_f32_e32 v4, v2, v3
	v_pk_mul_f32 v[2:3], v[16:17], v[178:179]
	v_mov_b32_e32 v179, v32
	v_add_f32_e32 v5, v2, v3
	v_mov_b32_e32 v2, v26
	v_mov_b32_e32 v3, v24
	v_pk_mul_f32 v[2:3], v[2:3], v[178:179]
	v_mov_b32_e32 v24, v27
	v_mov_b32_e32 v179, v33
	v_add_f32_e32 v16, v2, v3
	v_pk_mul_f32 v[2:3], v[24:25], v[178:179]
	v_mov_b32_e32 v179, v130
	v_add_f32_e32 v17, v2, v3
	v_mov_b32_e32 v2, v14
	v_mov_b32_e32 v3, v22
	v_pk_mul_f32 v[2:3], v[2:3], v[178:179]
	v_mov_b32_e32 v22, v15
	v_mov_b32_e32 v179, v131
	v_add_f32_e32 v28, v28, v29
	v_add_f32_e32 v14, v2, v3
	v_pk_mul_f32 v[2:3], v[22:23], v[178:179]
	v_mul_f32_e32 v4, 0x41800000, v4
	v_add_f32_e32 v15, v2, v3
	v_mul_f32_e32 v2, 0x41800000, v28
	v_mul_f32_e32 v3, 0x41800000, v9
	v_med3_f32 v9, v2, s57, v207
	v_med3_f32 v3, v3, s57, v207
	v_mov_b32_e32 v2, v167
	v_cvt_pk_fp8_f32 v2, v9, v3
	v_mul_f32_e32 v3, 0x41800000, v5
	v_med3_f32 v4, v4, s57, v207
	v_med3_f32 v3, v3, s57, v207
	v_cvt_pk_fp8_f32 v2, v4, v3 op_sel:[0,0,1]
	v_mul_f32_e32 v3, 0x41800000, v16
	v_mul_f32_e32 v4, 0x41800000, v17
	v_med3_f32 v9, v3, s57, v207
	v_med3_f32 v4, v4, s57, v207
	v_mov_b32_e32 v3, v167
	v_cvt_pk_fp8_f32 v3, v9, v4
	v_mul_f32_e32 v5, 0x41800000, v14
	v_mul_f32_e32 v4, 0x41800000, v15
	v_med3_f32 v5, v5, s57, v207
	v_med3_f32 v4, v4, s57, v207
	v_cvt_pk_fp8_f32 v3, v5, v4 op_sel:[0,0,1]
	v_add_u32_e32 v16, 32, v8
	v_ashrrev_i32_e32 v17, 31, v16
	v_pk_mul_f32 v[28:29], v[122:123], s[28:29] op_sel_hi:[1,0]
	global_store_dwordx2 v[18:19], v[2:3], off offset:128
	v_mad_i64_i32 v[2:3], s[0:1], v16, s56, v[10:11]
	v_lshl_add_u64 v[14:15], v[2:3], 0, v[12:13]
	v_lshlrev_b64 v[18:19], 11, v[16:17]
	v_lshl_add_u64 v[16:17], s[16:17], 0, v[18:19]
	v_lshl_add_u64 v[16:17], v[16:17], 0, v[6:7]
	v_pk_mul_f32 v[26:27], v[124:125], s[28:29] op_sel_hi:[1,0]
	v_pk_mul_f32 v[24:25], v[126:127], s[28:29] op_sel_hi:[1,0]
	v_pk_mul_f32 v[22:23], v[128:129], s[28:29] op_sel_hi:[1,0]
	s_waitcnt vmcnt(11)
	v_mov_b64_e32 v[2:3], v[230:231]
	v_mov_b64_e32 v[4:5], v[232:233]
	v_lshlrev_b32_e32 v9, 16, v2
	v_mul_f32_e32 v9, 0xbfb8aa3b, v9
	v_exp_f32_e32 v9, v9
	v_and_b32_e32 v2, 0xffff0000, v2
	v_mul_f32_e32 v2, 0xbfb8aa3b, v2
	v_exp_f32_e32 v2, v2
	v_add_f32_e32 v9, 1.0, v9
	v_add_f32_e32 v2, 1.0, v2
	v_lshlrev_b32_e32 v31, 16, v3
	v_mul_f32_e32 v31, 0xbfb8aa3b, v31
	v_rcp_f32_e32 v179, v9
	v_exp_f32_e32 v31, v31
	s_nop 0
	v_add_f32_e32 v31, 1.0, v31
	v_and_b32_e32 v3, 0xffff0000, v3
	v_mul_f32_e32 v3, 0xbfb8aa3b, v3
	v_rcp_f32_e32 v9, v2
	v_exp_f32_e32 v3, v3
	s_nop 0
	v_add_f32_e32 v3, 1.0, v3
	v_rcp_f32_e32 v123, v31
	v_lshlrev_b32_e32 v31, 16, v4
	v_mul_f32_e32 v31, 0xbfb8aa3b, v31
	v_exp_f32_e32 v31, v31
	s_nop 0
	v_add_f32_e32 v31, 1.0, v31
	v_and_b32_e32 v4, 0xffff0000, v4
	v_mul_f32_e32 v4, 0xbfb8aa3b, v4
	v_exp_f32_e32 v4, v4
	v_rcp_f32_e32 v122, v3
	v_add_f32_e32 v4, 1.0, v4
	v_rcp_f32_e32 v124, v31
	v_lshlrev_b32_e32 v31, 16, v5
	v_mul_f32_e32 v31, 0xbfb8aa3b, v31
	v_exp_f32_e32 v31, v31
	s_nop 0
	v_add_f32_e32 v30, 1.0, v31
	v_rcp_f32_e32 v125, v4
	v_and_b32_e32 v4, 0xffff0000, v5
	v_mul_f32_e32 v4, 0xbfb8aa3b, v4
	v_exp_f32_e32 v4, v4
	s_nop 0
	v_add_f32_e32 v4, 1.0, v4
	v_rcp_f32_e32 v126, v30
	v_mov_b32_e32 v33, v24
	v_rcp_f32_e32 v127, v4
	s_waitcnt vmcnt(10)
	v_mov_b64_e32 v[20:21], v[246:247]
	v_add_u32_e32 v250, 144, v8
	v_lshl_add_u32 v251, v250, 11, v6
	v_mad_u32_u24 v250, v250, s56, v12
	global_load_dwordx4 v[230:233], v250, s[18:19] nt
	global_load_dwordx2 v[246:247], v251, s[16:17]
	v_cvt_pk_f32_fp8_e32 v[2:3], v20
	v_cvt_pk_f32_fp8_sdwa v[4:5], v20 src0_sel:WORD_1
	v_cvt_pk_f32_fp8_e32 v[30:31], v21
	v_cvt_pk_f32_fp8_sdwa v[20:21], v21 src0_sel:WORD_1
	v_mov_b32_e32 v32, v2
	v_pk_mul_f32 v[32:33], v[32:33], v[178:179]
	v_mov_b32_e32 v24, v3
	v_mov_b32_e32 v179, v9
	v_pk_mul_f32 v[2:3], v[24:25], v[178:179]
	v_mov_b32_e32 v179, v123
	v_add_f32_e32 v9, v2, v3
	v_mov_b32_e32 v2, v4
	v_mov_b32_e32 v3, v22
	v_pk_mul_f32 v[2:3], v[2:3], v[178:179]
	v_mov_b32_e32 v22, v5
	v_mov_b32_e32 v179, v122
	v_add_f32_e32 v4, v2, v3
	v_pk_mul_f32 v[2:3], v[22:23], v[178:179]
	v_mov_b32_e32 v179, v124
	v_add_f32_e32 v5, v2, v3
	v_mov_b32_e32 v2, v30
	v_mov_b32_e32 v3, v28
	v_pk_mul_f32 v[2:3], v[2:3], v[178:179]
	v_mov_b32_e32 v28, v31
	v_mov_b32_e32 v179, v125
	v_add_f32_e32 v22, v2, v3
	v_pk_mul_f32 v[2:3], v[28:29], v[178:179]
	v_mov_b32_e32 v179, v126
	v_add_f32_e32 v23, v2, v3
	v_mov_b32_e32 v2, v20
	v_mov_b32_e32 v3, v26
	v_pk_mul_f32 v[2:3], v[2:3], v[178:179]
	v_mov_b32_e32 v26, v21
	v_mov_b32_e32 v179, v127
	v_add_f32_e32 v32, v32, v33
	v_add_f32_e32 v20, v2, v3
	v_pk_mul_f32 v[2:3], v[26:27], v[178:179]
	v_mul_f32_e32 v4, 0x41800000, v4
	v_add_f32_e32 v21, v2, v3
	v_mul_f32_e32 v2, 0x41800000, v32
	v_mul_f32_e32 v3, 0x41800000, v9
	v_med3_f32 v9, v2, s57, v207
	v_med3_f32 v3, v3, s57, v207
	v_mov_b32_e32 v2, v167
	v_cvt_pk_fp8_f32 v2, v9, v3
	v_mul_f32_e32 v3, 0x41800000, v5
	v_med3_f32 v4, v4, s57, v207
	v_med3_f32 v3, v3, s57, v207
	v_cvt_pk_fp8_f32 v2, v4, v3 op_sel:[0,0,1]
	v_mul_f32_e32 v3, 0x41800000, v22
	v_mul_f32_e32 v4, 0x41800000, v23
	v_med3_f32 v9, v3, s57, v207
	v_med3_f32 v4, v4, s57, v207
	v_mov_b32_e32 v3, v167
	v_cvt_pk_fp8_f32 v3, v9, v4
	v_mul_f32_e32 v5, 0x41800000, v20
	v_mul_f32_e32 v4, 0x41800000, v21
	v_med3_f32 v5, v5, s57, v207
	v_med3_f32 v4, v4, s57, v207
	v_cvt_pk_fp8_f32 v3, v5, v4 op_sel:[0,0,1]
	v_lshl_add_u64 v[4:5], s[20:21], 0, v[18:19]
	v_lshl_add_u64 v[18:19], v[4:5], 0, v[6:7]
	v_pk_mul_f32 v[24:25], v[114:115], s[28:29] op_sel_hi:[1,0]
	global_store_dwordx2 v[18:19], v[2:3], off
	s_nop 0
	v_pk_mul_f32 v[20:21], v[118:119], s[28:29] op_sel_hi:[1,0]
	v_pk_mul_f32 v[16:17], v[120:121], s[28:29] op_sel_hi:[1,0]
	v_pk_mul_f32 v[22:23], v[116:117], s[28:29] op_sel_hi:[1,0]
	s_waitcnt vmcnt(11)
	v_mov_b64_e32 v[2:3], v[234:235]
	v_mov_b64_e32 v[4:5], v[236:237]
	v_lshlrev_b32_e32 v9, 16, v2
	v_mul_f32_e32 v9, 0xbfb8aa3b, v9
	v_exp_f32_e32 v9, v9
	v_and_b32_e32 v2, 0xffff0000, v2
	v_mul_f32_e32 v2, 0xbfb8aa3b, v2
	v_exp_f32_e32 v2, v2
	v_add_f32_e32 v9, 1.0, v9
	v_add_f32_e32 v2, 1.0, v2
	v_lshlrev_b32_e32 v27, 16, v3
	v_mul_f32_e32 v27, 0xbfb8aa3b, v27
	v_rcp_f32_e32 v179, v9
	v_exp_f32_e32 v27, v27
	s_nop 0
	v_add_f32_e32 v27, 1.0, v27
	v_and_b32_e32 v3, 0xffff0000, v3
	v_mul_f32_e32 v3, 0xbfb8aa3b, v3
	v_rcp_f32_e32 v9, v2
	v_exp_f32_e32 v3, v3
	s_nop 0
	v_add_f32_e32 v3, 1.0, v3
	v_rcp_f32_e32 v31, v27
	v_lshlrev_b32_e32 v27, 16, v4
	v_mul_f32_e32 v27, 0xbfb8aa3b, v27
	v_exp_f32_e32 v27, v27
	s_nop 0
	v_add_f32_e32 v27, 1.0, v27
	v_and_b32_e32 v4, 0xffff0000, v4
	v_mul_f32_e32 v4, 0xbfb8aa3b, v4
	v_exp_f32_e32 v4, v4
	v_rcp_f32_e32 v30, v3
	v_add_f32_e32 v4, 1.0, v4
	v_rcp_f32_e32 v32, v27
	v_lshlrev_b32_e32 v27, 16, v5
	v_mul_f32_e32 v27, 0xbfb8aa3b, v27
	v_exp_f32_e32 v27, v27
	s_nop 0
	v_add_f32_e32 v26, 1.0, v27
	v_rcp_f32_e32 v33, v4
	v_and_b32_e32 v4, 0xffff0000, v5
	v_mul_f32_e32 v4, 0xbfb8aa3b, v4
	v_exp_f32_e32 v4, v4
	s_nop 0
	v_add_f32_e32 v4, 1.0, v4
	v_rcp_f32_e32 v114, v26
	v_mov_b32_e32 v29, v20
	v_rcp_f32_e32 v115, v4
	s_waitcnt vmcnt(10)
	v_mov_b64_e32 v[14:15], v[248:249]
	v_add_u32_e32 v250, 144, v8
	v_lshl_add_u32 v251, v250, 11, v6
	v_mad_u32_u24 v250, v250, s56, v12
	global_load_dwordx4 v[234:237], v250, s[18:19] offset:256 nt
	global_load_dwordx2 v[248:249], v251, s[16:17] offset:128
	v_cvt_pk_f32_fp8_e32 v[2:3], v14
	v_cvt_pk_f32_fp8_sdwa v[4:5], v14 src0_sel:WORD_1
	v_cvt_pk_f32_fp8_e32 v[26:27], v15
	v_cvt_pk_f32_fp8_sdwa v[14:15], v15 src0_sel:WORD_1
	v_mov_b32_e32 v28, v2
	v_pk_mul_f32 v[28:29], v[28:29], v[178:179]
	v_mov_b32_e32 v20, v3
	v_mov_b32_e32 v179, v9
	v_pk_mul_f32 v[2:3], v[20:21], v[178:179]
	v_mov_b32_e32 v179, v31
	v_add_f32_e32 v9, v2, v3
	v_mov_b32_e32 v2, v4
	v_mov_b32_e32 v3, v16
	v_pk_mul_f32 v[2:3], v[2:3], v[178:179]
	v_mov_b32_e32 v16, v5
	v_mov_b32_e32 v179, v30
	v_add_f32_e32 v4, v2, v3
	v_pk_mul_f32 v[2:3], v[16:17], v[178:179]
	v_mov_b32_e32 v179, v32
	v_add_f32_e32 v5, v2, v3
	v_mov_b32_e32 v2, v26
	v_mov_b32_e32 v3, v24
	v_pk_mul_f32 v[2:3], v[2:3], v[178:179]
	v_mov_b32_e32 v24, v27
	v_mov_b32_e32 v179, v33
	v_add_f32_e32 v16, v2, v3
	v_pk_mul_f32 v[2:3], v[24:25], v[178:179]
	v_mov_b32_e32 v179, v114
	v_add_f32_e32 v17, v2, v3
	v_mov_b32_e32 v2, v14
	v_mov_b32_e32 v3, v22
	v_pk_mul_f32 v[2:3], v[2:3], v[178:179]
	v_mov_b32_e32 v22, v15
	v_mov_b32_e32 v179, v115
	v_add_f32_e32 v28, v28, v29
	v_add_f32_e32 v14, v2, v3
	v_pk_mul_f32 v[2:3], v[22:23], v[178:179]
	v_mul_f32_e32 v4, 0x41800000, v4
	v_add_f32_e32 v15, v2, v3
	v_mul_f32_e32 v2, 0x41800000, v28
	v_mul_f32_e32 v3, 0x41800000, v9
	v_med3_f32 v9, v2, s57, v207
	v_med3_f32 v3, v3, s57, v207
	v_mov_b32_e32 v2, v167
	v_cvt_pk_fp8_f32 v2, v9, v3
	v_mul_f32_e32 v3, 0x41800000, v5
	v_med3_f32 v4, v4, s57, v207
	v_med3_f32 v3, v3, s57, v207
	v_cvt_pk_fp8_f32 v2, v4, v3 op_sel:[0,0,1]
	v_mul_f32_e32 v3, 0x41800000, v16
	v_mul_f32_e32 v4, 0x41800000, v17
	v_med3_f32 v9, v3, s57, v207
	v_med3_f32 v4, v4, s57, v207
	v_mov_b32_e32 v3, v167
	v_cvt_pk_fp8_f32 v3, v9, v4
	v_mul_f32_e32 v5, 0x41800000, v14
	v_mul_f32_e32 v4, 0x41800000, v15
	v_med3_f32 v5, v5, s57, v207
	v_med3_f32 v4, v4, s57, v207
	v_cvt_pk_fp8_f32 v3, v5, v4 op_sel:[0,0,1]
	v_add_u32_e32 v16, 48, v8
	v_ashrrev_i32_e32 v17, 31, v16
	v_pk_mul_f32 v[28:29], v[106:107], s[28:29] op_sel_hi:[1,0]
	global_store_dwordx2 v[18:19], v[2:3], off offset:128
	v_mad_i64_i32 v[2:3], s[0:1], v16, s56, v[10:11]
	v_lshl_add_u64 v[14:15], v[2:3], 0, v[12:13]
	v_lshlrev_b64 v[18:19], 11, v[16:17]
	v_lshl_add_u64 v[16:17], s[16:17], 0, v[18:19]
	v_lshl_add_u64 v[16:17], v[16:17], 0, v[6:7]
	v_pk_mul_f32 v[26:27], v[108:109], s[28:29] op_sel_hi:[1,0]
	v_pk_mul_f32 v[24:25], v[110:111], s[28:29] op_sel_hi:[1,0]
	v_pk_mul_f32 v[22:23], v[112:113], s[28:29] op_sel_hi:[1,0]
	s_waitcnt vmcnt(11)
	v_mov_b64_e32 v[2:3], v[214:215]
	v_mov_b64_e32 v[4:5], v[216:217]
	v_lshlrev_b32_e32 v9, 16, v2
	v_mul_f32_e32 v9, 0xbfb8aa3b, v9
	v_exp_f32_e32 v9, v9
	v_and_b32_e32 v2, 0xffff0000, v2
	v_mul_f32_e32 v2, 0xbfb8aa3b, v2
	v_exp_f32_e32 v2, v2
	v_add_f32_e32 v9, 1.0, v9
	v_add_f32_e32 v2, 1.0, v2
	v_lshlrev_b32_e32 v31, 16, v3
	v_mul_f32_e32 v31, 0xbfb8aa3b, v31
	v_rcp_f32_e32 v179, v9
	v_exp_f32_e32 v31, v31
	s_nop 0
	v_add_f32_e32 v31, 1.0, v31
	v_and_b32_e32 v3, 0xffff0000, v3
	v_mul_f32_e32 v3, 0xbfb8aa3b, v3
	v_rcp_f32_e32 v9, v2
	v_exp_f32_e32 v3, v3
	s_nop 0
	v_add_f32_e32 v3, 1.0, v3
	v_rcp_f32_e32 v107, v31
	v_lshlrev_b32_e32 v31, 16, v4
	v_mul_f32_e32 v31, 0xbfb8aa3b, v31
	v_exp_f32_e32 v31, v31
	s_nop 0
	v_add_f32_e32 v31, 1.0, v31
	v_and_b32_e32 v4, 0xffff0000, v4
	v_mul_f32_e32 v4, 0xbfb8aa3b, v4
	v_exp_f32_e32 v4, v4
	v_rcp_f32_e32 v106, v3
	v_add_f32_e32 v4, 1.0, v4
	v_rcp_f32_e32 v108, v31
	v_lshlrev_b32_e32 v31, 16, v5
	v_mul_f32_e32 v31, 0xbfb8aa3b, v31
	v_exp_f32_e32 v31, v31
	s_nop 0
	v_add_f32_e32 v30, 1.0, v31
	v_rcp_f32_e32 v109, v4
	v_and_b32_e32 v4, 0xffff0000, v5
	v_mul_f32_e32 v4, 0xbfb8aa3b, v4
	v_exp_f32_e32 v4, v4
	s_nop 0
	v_add_f32_e32 v4, 1.0, v4
	v_rcp_f32_e32 v110, v30
	v_mov_b32_e32 v33, v24
	v_rcp_f32_e32 v111, v4
	s_waitcnt vmcnt(10)
	v_mov_b64_e32 v[20:21], v[238:239]
	v_add_u32_e32 v250, 160, v8
	v_lshl_add_u32 v251, v250, 11, v6
	v_mad_u32_u24 v250, v250, s56, v12
	global_load_dwordx4 v[214:217], v250, s[18:19] nt
	global_load_dwordx2 v[238:239], v251, s[16:17]
	v_cvt_pk_f32_fp8_e32 v[2:3], v20
	v_cvt_pk_f32_fp8_sdwa v[4:5], v20 src0_sel:WORD_1
	v_cvt_pk_f32_fp8_e32 v[30:31], v21
	v_cvt_pk_f32_fp8_sdwa v[20:21], v21 src0_sel:WORD_1
	v_mov_b32_e32 v32, v2
	v_pk_mul_f32 v[32:33], v[32:33], v[178:179]
	v_mov_b32_e32 v24, v3
	v_mov_b32_e32 v179, v9
	v_pk_mul_f32 v[2:3], v[24:25], v[178:179]
	v_mov_b32_e32 v179, v107
	v_add_f32_e32 v9, v2, v3
	v_mov_b32_e32 v2, v4
	v_mov_b32_e32 v3, v22
	v_pk_mul_f32 v[2:3], v[2:3], v[178:179]
	v_mov_b32_e32 v22, v5
	v_mov_b32_e32 v179, v106
	v_add_f32_e32 v4, v2, v3
	v_pk_mul_f32 v[2:3], v[22:23], v[178:179]
	v_mov_b32_e32 v179, v108
	v_add_f32_e32 v5, v2, v3
	v_mov_b32_e32 v2, v30
	v_mov_b32_e32 v3, v28
	v_pk_mul_f32 v[2:3], v[2:3], v[178:179]
	v_mov_b32_e32 v28, v31
	v_mov_b32_e32 v179, v109
	v_add_f32_e32 v22, v2, v3
	v_pk_mul_f32 v[2:3], v[28:29], v[178:179]
	v_mov_b32_e32 v179, v110
	v_add_f32_e32 v23, v2, v3
	v_mov_b32_e32 v2, v20
	v_mov_b32_e32 v3, v26
	v_pk_mul_f32 v[2:3], v[2:3], v[178:179]
	v_mov_b32_e32 v26, v21
	v_mov_b32_e32 v179, v111
	v_add_f32_e32 v32, v32, v33
	v_add_f32_e32 v20, v2, v3
	v_pk_mul_f32 v[2:3], v[26:27], v[178:179]
	v_mul_f32_e32 v4, 0x41800000, v4
	v_add_f32_e32 v21, v2, v3
	v_mul_f32_e32 v2, 0x41800000, v32
	v_mul_f32_e32 v3, 0x41800000, v9
	v_med3_f32 v9, v2, s57, v207
	v_med3_f32 v3, v3, s57, v207
	v_mov_b32_e32 v2, v167
	v_cvt_pk_fp8_f32 v2, v9, v3
	v_mul_f32_e32 v3, 0x41800000, v5
	v_med3_f32 v4, v4, s57, v207
	v_med3_f32 v3, v3, s57, v207
	v_cvt_pk_fp8_f32 v2, v4, v3 op_sel:[0,0,1]
	v_mul_f32_e32 v3, 0x41800000, v22
	v_mul_f32_e32 v4, 0x41800000, v23
	v_med3_f32 v9, v3, s57, v207
	v_med3_f32 v4, v4, s57, v207
	v_mov_b32_e32 v3, v167
	v_cvt_pk_fp8_f32 v3, v9, v4
	v_mul_f32_e32 v5, 0x41800000, v20
	v_mul_f32_e32 v4, 0x41800000, v21
	v_med3_f32 v5, v5, s57, v207
	v_med3_f32 v4, v4, s57, v207
	v_cvt_pk_fp8_f32 v3, v5, v4 op_sel:[0,0,1]
	v_lshl_add_u64 v[4:5], s[20:21], 0, v[18:19]
	v_lshl_add_u64 v[18:19], v[4:5], 0, v[6:7]
	v_pk_mul_f32 v[24:25], v[98:99], s[28:29] op_sel_hi:[1,0]
	global_store_dwordx2 v[18:19], v[2:3], off
	s_nop 0
	v_pk_mul_f32 v[20:21], v[102:103], s[28:29] op_sel_hi:[1,0]
	v_pk_mul_f32 v[16:17], v[104:105], s[28:29] op_sel_hi:[1,0]
	v_pk_mul_f32 v[22:23], v[100:101], s[28:29] op_sel_hi:[1,0]
	s_waitcnt vmcnt(11)
	v_mov_b64_e32 v[2:3], v[218:219]
	v_mov_b64_e32 v[4:5], v[220:221]
	v_lshlrev_b32_e32 v9, 16, v2
	v_mul_f32_e32 v9, 0xbfb8aa3b, v9
	v_exp_f32_e32 v9, v9
	v_and_b32_e32 v2, 0xffff0000, v2
	v_mul_f32_e32 v2, 0xbfb8aa3b, v2
	v_exp_f32_e32 v2, v2
	v_add_f32_e32 v9, 1.0, v9
	v_add_f32_e32 v2, 1.0, v2
	v_lshlrev_b32_e32 v27, 16, v3
	v_mul_f32_e32 v27, 0xbfb8aa3b, v27
	v_rcp_f32_e32 v179, v9
	v_exp_f32_e32 v27, v27
	s_nop 0
	v_add_f32_e32 v27, 1.0, v27
	v_and_b32_e32 v3, 0xffff0000, v3
	v_mul_f32_e32 v3, 0xbfb8aa3b, v3
	v_rcp_f32_e32 v9, v2
	v_exp_f32_e32 v3, v3
	s_nop 0
	v_add_f32_e32 v3, 1.0, v3
	v_rcp_f32_e32 v31, v27
	v_lshlrev_b32_e32 v27, 16, v4
	v_mul_f32_e32 v27, 0xbfb8aa3b, v27
	v_exp_f32_e32 v27, v27
	s_nop 0
	v_add_f32_e32 v27, 1.0, v27
	v_and_b32_e32 v4, 0xffff0000, v4
	v_mul_f32_e32 v4, 0xbfb8aa3b, v4
	v_exp_f32_e32 v4, v4
	v_rcp_f32_e32 v30, v3
	v_add_f32_e32 v4, 1.0, v4
	v_rcp_f32_e32 v32, v27
	v_lshlrev_b32_e32 v27, 16, v5
	v_mul_f32_e32 v27, 0xbfb8aa3b, v27
	v_exp_f32_e32 v27, v27
	s_nop 0
	v_add_f32_e32 v26, 1.0, v27
	v_rcp_f32_e32 v33, v4
	v_and_b32_e32 v4, 0xffff0000, v5
	v_mul_f32_e32 v4, 0xbfb8aa3b, v4
	v_exp_f32_e32 v4, v4
	s_nop 0
	v_add_f32_e32 v4, 1.0, v4
	v_rcp_f32_e32 v98, v26
	v_mov_b32_e32 v29, v20
	v_rcp_f32_e32 v99, v4
	s_waitcnt vmcnt(10)
	v_mov_b64_e32 v[14:15], v[240:241]
	v_add_u32_e32 v250, 160, v8
	v_lshl_add_u32 v251, v250, 11, v6
	v_mad_u32_u24 v250, v250, s56, v12
	global_load_dwordx4 v[218:221], v250, s[18:19] offset:256 nt
	global_load_dwordx2 v[240:241], v251, s[16:17] offset:128
	v_cvt_pk_f32_fp8_e32 v[2:3], v14
	v_cvt_pk_f32_fp8_sdwa v[4:5], v14 src0_sel:WORD_1
	v_cvt_pk_f32_fp8_e32 v[26:27], v15
	v_cvt_pk_f32_fp8_sdwa v[14:15], v15 src0_sel:WORD_1
	v_mov_b32_e32 v28, v2
	v_pk_mul_f32 v[28:29], v[28:29], v[178:179]
	v_mov_b32_e32 v20, v3
	v_mov_b32_e32 v179, v9
	v_pk_mul_f32 v[2:3], v[20:21], v[178:179]
	v_mov_b32_e32 v179, v31
	v_add_f32_e32 v9, v2, v3
	v_mov_b32_e32 v2, v4
	v_mov_b32_e32 v3, v16
	v_pk_mul_f32 v[2:3], v[2:3], v[178:179]
	v_mov_b32_e32 v16, v5
	v_mov_b32_e32 v179, v30
	v_add_f32_e32 v4, v2, v3
	v_pk_mul_f32 v[2:3], v[16:17], v[178:179]
	v_mov_b32_e32 v179, v32
	v_add_f32_e32 v5, v2, v3
	v_mov_b32_e32 v2, v26
	v_mov_b32_e32 v3, v24
	v_pk_mul_f32 v[2:3], v[2:3], v[178:179]
	v_mov_b32_e32 v24, v27
	v_mov_b32_e32 v179, v33
	v_add_f32_e32 v16, v2, v3
	v_pk_mul_f32 v[2:3], v[24:25], v[178:179]
	v_mov_b32_e32 v179, v98
	v_add_f32_e32 v17, v2, v3
	v_mov_b32_e32 v2, v14
	v_mov_b32_e32 v3, v22
	v_pk_mul_f32 v[2:3], v[2:3], v[178:179]
	v_mov_b32_e32 v22, v15
	v_mov_b32_e32 v179, v99
	v_add_f32_e32 v28, v28, v29
	v_add_f32_e32 v14, v2, v3
	v_pk_mul_f32 v[2:3], v[22:23], v[178:179]
	v_mul_f32_e32 v4, 0x41800000, v4
	v_add_f32_e32 v15, v2, v3
	v_mul_f32_e32 v2, 0x41800000, v28
	v_mul_f32_e32 v3, 0x41800000, v9
	v_med3_f32 v9, v2, s57, v207
	v_med3_f32 v3, v3, s57, v207
	v_mov_b32_e32 v2, v167
	v_cvt_pk_fp8_f32 v2, v9, v3
	v_mul_f32_e32 v3, 0x41800000, v5
	v_med3_f32 v4, v4, s57, v207
	v_med3_f32 v3, v3, s57, v207
	v_cvt_pk_fp8_f32 v2, v4, v3 op_sel:[0,0,1]
	v_mul_f32_e32 v3, 0x41800000, v16
	v_mul_f32_e32 v4, 0x41800000, v17
	v_med3_f32 v9, v3, s57, v207
	v_med3_f32 v4, v4, s57, v207
	v_mov_b32_e32 v3, v167
	v_cvt_pk_fp8_f32 v3, v9, v4
	v_mul_f32_e32 v5, 0x41800000, v14
	v_mul_f32_e32 v4, 0x41800000, v15
	v_med3_f32 v5, v5, s57, v207
	v_med3_f32 v4, v4, s57, v207
	v_cvt_pk_fp8_f32 v3, v5, v4 op_sel:[0,0,1]
	v_add_u32_e32 v16, 0x80, v8
	v_ashrrev_i32_e32 v17, 31, v16
	v_pk_mul_f32 v[28:29], v[90:91], s[28:29] op_sel_hi:[1,0]
	global_store_dwordx2 v[18:19], v[2:3], off offset:128
	v_mad_i64_i32 v[2:3], s[0:1], v16, s56, v[10:11]
	v_lshl_add_u64 v[14:15], v[2:3], 0, v[12:13]
	v_lshlrev_b64 v[18:19], 11, v[16:17]
	v_lshl_add_u64 v[16:17], s[16:17], 0, v[18:19]
	v_lshl_add_u64 v[16:17], v[16:17], 0, v[6:7]
	v_pk_mul_f32 v[26:27], v[92:93], s[28:29] op_sel_hi:[1,0]
	v_pk_mul_f32 v[24:25], v[94:95], s[28:29] op_sel_hi:[1,0]
	v_pk_mul_f32 v[22:23], v[96:97], s[28:29] op_sel_hi:[1,0]
	s_waitcnt vmcnt(11)
	v_mov_b64_e32 v[2:3], v[222:223]
	v_mov_b64_e32 v[4:5], v[224:225]
	v_lshlrev_b32_e32 v9, 16, v2
	v_mul_f32_e32 v9, 0xbfb8aa3b, v9
	v_exp_f32_e32 v9, v9
	v_and_b32_e32 v2, 0xffff0000, v2
	v_mul_f32_e32 v2, 0xbfb8aa3b, v2
	v_exp_f32_e32 v2, v2
	v_add_f32_e32 v9, 1.0, v9
	v_add_f32_e32 v2, 1.0, v2
	v_lshlrev_b32_e32 v31, 16, v3
	v_mul_f32_e32 v31, 0xbfb8aa3b, v31
	v_rcp_f32_e32 v179, v9
	v_exp_f32_e32 v31, v31
	s_nop 0
	v_add_f32_e32 v31, 1.0, v31
	v_and_b32_e32 v3, 0xffff0000, v3
	v_mul_f32_e32 v3, 0xbfb8aa3b, v3
	v_rcp_f32_e32 v9, v2
	v_exp_f32_e32 v3, v3
	s_nop 0
	v_add_f32_e32 v3, 1.0, v3
	v_rcp_f32_e32 v91, v31
	v_lshlrev_b32_e32 v31, 16, v4
	v_mul_f32_e32 v31, 0xbfb8aa3b, v31
	v_exp_f32_e32 v31, v31
	s_nop 0
	v_add_f32_e32 v31, 1.0, v31
	v_and_b32_e32 v4, 0xffff0000, v4
	v_mul_f32_e32 v4, 0xbfb8aa3b, v4
	v_exp_f32_e32 v4, v4
	v_rcp_f32_e32 v90, v3
	v_add_f32_e32 v4, 1.0, v4
	v_rcp_f32_e32 v92, v31
	v_lshlrev_b32_e32 v31, 16, v5
	v_mul_f32_e32 v31, 0xbfb8aa3b, v31
	v_exp_f32_e32 v31, v31
	s_nop 0
	v_add_f32_e32 v30, 1.0, v31
	v_rcp_f32_e32 v93, v4
	v_and_b32_e32 v4, 0xffff0000, v5
	v_mul_f32_e32 v4, 0xbfb8aa3b, v4
	v_exp_f32_e32 v4, v4
	s_nop 0
	v_add_f32_e32 v4, 1.0, v4
	v_rcp_f32_e32 v94, v30
	v_mov_b32_e32 v33, v24
	v_rcp_f32_e32 v95, v4
	s_waitcnt vmcnt(10)
	v_mov_b64_e32 v[20:21], v[242:243]
	v_add_u32_e32 v250, 176, v8
	v_lshl_add_u32 v251, v250, 11, v6
	v_mad_u32_u24 v250, v250, s56, v12
	global_load_dwordx4 v[222:225], v250, s[18:19] nt
	global_load_dwordx2 v[242:243], v251, s[16:17]
	v_cvt_pk_f32_fp8_e32 v[2:3], v20
	v_cvt_pk_f32_fp8_sdwa v[4:5], v20 src0_sel:WORD_1
	v_cvt_pk_f32_fp8_e32 v[30:31], v21
	v_cvt_pk_f32_fp8_sdwa v[20:21], v21 src0_sel:WORD_1
	v_mov_b32_e32 v32, v2
	v_pk_mul_f32 v[32:33], v[32:33], v[178:179]
	v_mov_b32_e32 v24, v3
	v_mov_b32_e32 v179, v9
	v_pk_mul_f32 v[2:3], v[24:25], v[178:179]
	v_mov_b32_e32 v179, v91
	v_add_f32_e32 v9, v2, v3
	v_mov_b32_e32 v2, v4
	v_mov_b32_e32 v3, v22
	v_pk_mul_f32 v[2:3], v[2:3], v[178:179]
	v_mov_b32_e32 v22, v5
	v_mov_b32_e32 v179, v90
	v_add_f32_e32 v4, v2, v3
	v_pk_mul_f32 v[2:3], v[22:23], v[178:179]
	v_mov_b32_e32 v179, v92
	v_add_f32_e32 v5, v2, v3
	v_mov_b32_e32 v2, v30
	v_mov_b32_e32 v3, v28
	v_pk_mul_f32 v[2:3], v[2:3], v[178:179]
	v_mov_b32_e32 v28, v31
	v_mov_b32_e32 v179, v93
	v_add_f32_e32 v22, v2, v3
	v_pk_mul_f32 v[2:3], v[28:29], v[178:179]
	v_mov_b32_e32 v179, v94
	v_add_f32_e32 v23, v2, v3
	v_mov_b32_e32 v2, v20
	v_mov_b32_e32 v3, v26
	v_pk_mul_f32 v[2:3], v[2:3], v[178:179]
	v_mov_b32_e32 v26, v21
	v_mov_b32_e32 v179, v95
	v_add_f32_e32 v32, v32, v33
	v_add_f32_e32 v20, v2, v3
	v_pk_mul_f32 v[2:3], v[26:27], v[178:179]
	v_mul_f32_e32 v4, 0x41800000, v4
	v_add_f32_e32 v21, v2, v3
	v_mul_f32_e32 v2, 0x41800000, v32
	v_mul_f32_e32 v3, 0x41800000, v9
	v_med3_f32 v9, v2, s57, v207
	v_med3_f32 v3, v3, s57, v207
	v_mov_b32_e32 v2, v167
	v_cvt_pk_fp8_f32 v2, v9, v3
	v_mul_f32_e32 v3, 0x41800000, v5
	v_med3_f32 v4, v4, s57, v207
	v_med3_f32 v3, v3, s57, v207
	v_cvt_pk_fp8_f32 v2, v4, v3 op_sel:[0,0,1]
	v_mul_f32_e32 v3, 0x41800000, v22
	v_mul_f32_e32 v4, 0x41800000, v23
	v_med3_f32 v9, v3, s57, v207
	v_med3_f32 v4, v4, s57, v207
	v_mov_b32_e32 v3, v167
	v_cvt_pk_fp8_f32 v3, v9, v4
	v_mul_f32_e32 v5, 0x41800000, v20
	v_mul_f32_e32 v4, 0x41800000, v21
	v_med3_f32 v5, v5, s57, v207
	v_med3_f32 v4, v4, s57, v207
	v_cvt_pk_fp8_f32 v3, v5, v4 op_sel:[0,0,1]
	v_lshl_add_u64 v[4:5], s[20:21], 0, v[18:19]
	v_lshl_add_u64 v[18:19], v[4:5], 0, v[6:7]
	v_pk_mul_f32 v[24:25], v[82:83], s[28:29] op_sel_hi:[1,0]
	global_store_dwordx2 v[18:19], v[2:3], off
	s_nop 0
	v_pk_mul_f32 v[20:21], v[86:87], s[28:29] op_sel_hi:[1,0]
	v_pk_mul_f32 v[16:17], v[88:89], s[28:29] op_sel_hi:[1,0]
	v_pk_mul_f32 v[22:23], v[84:85], s[28:29] op_sel_hi:[1,0]
	s_waitcnt vmcnt(11)
	v_mov_b64_e32 v[2:3], v[226:227]
	v_mov_b64_e32 v[4:5], v[228:229]
	v_lshlrev_b32_e32 v9, 16, v2
	v_mul_f32_e32 v9, 0xbfb8aa3b, v9
	v_exp_f32_e32 v9, v9
	v_and_b32_e32 v2, 0xffff0000, v2
	v_mul_f32_e32 v2, 0xbfb8aa3b, v2
	v_exp_f32_e32 v2, v2
	v_add_f32_e32 v9, 1.0, v9
	v_add_f32_e32 v2, 1.0, v2
	v_lshlrev_b32_e32 v27, 16, v3
	v_mul_f32_e32 v27, 0xbfb8aa3b, v27
	v_rcp_f32_e32 v179, v9
	v_exp_f32_e32 v27, v27
	s_nop 0
	v_add_f32_e32 v27, 1.0, v27
	v_and_b32_e32 v3, 0xffff0000, v3
	v_mul_f32_e32 v3, 0xbfb8aa3b, v3
	v_rcp_f32_e32 v9, v2
	v_exp_f32_e32 v3, v3
	s_nop 0
	v_add_f32_e32 v3, 1.0, v3
	v_rcp_f32_e32 v31, v27
	v_lshlrev_b32_e32 v27, 16, v4
	v_mul_f32_e32 v27, 0xbfb8aa3b, v27
	v_exp_f32_e32 v27, v27
	s_nop 0
	v_add_f32_e32 v27, 1.0, v27
	v_and_b32_e32 v4, 0xffff0000, v4
	v_mul_f32_e32 v4, 0xbfb8aa3b, v4
	v_exp_f32_e32 v4, v4
	v_rcp_f32_e32 v30, v3
	v_add_f32_e32 v4, 1.0, v4
	v_rcp_f32_e32 v32, v27
	v_lshlrev_b32_e32 v27, 16, v5
	v_mul_f32_e32 v27, 0xbfb8aa3b, v27
	v_exp_f32_e32 v27, v27
	s_nop 0
	v_add_f32_e32 v26, 1.0, v27
	v_rcp_f32_e32 v33, v4
	v_and_b32_e32 v4, 0xffff0000, v5
	v_mul_f32_e32 v4, 0xbfb8aa3b, v4
	v_exp_f32_e32 v4, v4
	s_nop 0
	v_add_f32_e32 v4, 1.0, v4
	v_rcp_f32_e32 v82, v26
	v_mov_b32_e32 v29, v20
	v_rcp_f32_e32 v83, v4
	s_waitcnt vmcnt(10)
	v_mov_b64_e32 v[14:15], v[244:245]
	v_add_u32_e32 v250, 176, v8
	v_lshl_add_u32 v251, v250, 11, v6
	v_mad_u32_u24 v250, v250, s56, v12
	global_load_dwordx4 v[226:229], v250, s[18:19] offset:256 nt
	global_load_dwordx2 v[244:245], v251, s[16:17] offset:128
	v_cvt_pk_f32_fp8_e32 v[2:3], v14
	v_cvt_pk_f32_fp8_sdwa v[4:5], v14 src0_sel:WORD_1
	v_cvt_pk_f32_fp8_e32 v[26:27], v15
	v_cvt_pk_f32_fp8_sdwa v[14:15], v15 src0_sel:WORD_1
	v_mov_b32_e32 v28, v2
	v_pk_mul_f32 v[28:29], v[28:29], v[178:179]
	v_mov_b32_e32 v20, v3
	v_mov_b32_e32 v179, v9
	v_pk_mul_f32 v[2:3], v[20:21], v[178:179]
	v_mov_b32_e32 v179, v31
	v_add_f32_e32 v9, v2, v3
	v_mov_b32_e32 v2, v4
	v_mov_b32_e32 v3, v16
	v_pk_mul_f32 v[2:3], v[2:3], v[178:179]
	v_mov_b32_e32 v16, v5
	v_mov_b32_e32 v179, v30
	v_add_f32_e32 v4, v2, v3
	v_pk_mul_f32 v[2:3], v[16:17], v[178:179]
	v_mov_b32_e32 v179, v32
	v_add_f32_e32 v5, v2, v3
	v_mov_b32_e32 v2, v26
	v_mov_b32_e32 v3, v24
	v_pk_mul_f32 v[2:3], v[2:3], v[178:179]
	v_mov_b32_e32 v24, v27
	v_mov_b32_e32 v179, v33
	v_add_f32_e32 v16, v2, v3
	v_pk_mul_f32 v[2:3], v[24:25], v[178:179]
	v_mov_b32_e32 v179, v82
	v_add_f32_e32 v17, v2, v3
	v_mov_b32_e32 v2, v14
	v_mov_b32_e32 v3, v22
	v_pk_mul_f32 v[2:3], v[2:3], v[178:179]
	v_mov_b32_e32 v22, v15
	v_mov_b32_e32 v179, v83
	v_add_f32_e32 v28, v28, v29
	v_add_f32_e32 v14, v2, v3
	v_pk_mul_f32 v[2:3], v[22:23], v[178:179]
	v_mul_f32_e32 v4, 0x41800000, v4
	v_add_f32_e32 v15, v2, v3
	v_mul_f32_e32 v2, 0x41800000, v28
	v_mul_f32_e32 v3, 0x41800000, v9
	v_med3_f32 v9, v2, s57, v207
	v_med3_f32 v3, v3, s57, v207
	v_mov_b32_e32 v2, v167
	v_cvt_pk_fp8_f32 v2, v9, v3
	v_mul_f32_e32 v3, 0x41800000, v5
	v_med3_f32 v4, v4, s57, v207
	v_med3_f32 v3, v3, s57, v207
	v_cvt_pk_fp8_f32 v2, v4, v3 op_sel:[0,0,1]
	v_mul_f32_e32 v3, 0x41800000, v16
	v_mul_f32_e32 v4, 0x41800000, v17
	v_med3_f32 v9, v3, s57, v207
	v_med3_f32 v4, v4, s57, v207
	v_mov_b32_e32 v3, v167
	v_cvt_pk_fp8_f32 v3, v9, v4
	v_mul_f32_e32 v5, 0x41800000, v14
	v_mul_f32_e32 v4, 0x41800000, v15
	v_med3_f32 v5, v5, s57, v207
	v_med3_f32 v4, v4, s57, v207
	v_cvt_pk_fp8_f32 v3, v5, v4 op_sel:[0,0,1]
	v_add_u32_e32 v16, 0x90, v8
	v_ashrrev_i32_e32 v17, 31, v16
	v_pk_mul_f32 v[28:29], v[74:75], s[28:29] op_sel_hi:[1,0]
	global_store_dwordx2 v[18:19], v[2:3], off offset:128
	v_mad_i64_i32 v[2:3], s[0:1], v16, s56, v[10:11]
	v_lshl_add_u64 v[14:15], v[2:3], 0, v[12:13]
	v_lshlrev_b64 v[18:19], 11, v[16:17]
	v_lshl_add_u64 v[16:17], s[16:17], 0, v[18:19]
	v_lshl_add_u64 v[16:17], v[16:17], 0, v[6:7]
	v_pk_mul_f32 v[26:27], v[76:77], s[28:29] op_sel_hi:[1,0]
	v_pk_mul_f32 v[24:25], v[78:79], s[28:29] op_sel_hi:[1,0]
	v_pk_mul_f32 v[22:23], v[80:81], s[28:29] op_sel_hi:[1,0]
	s_waitcnt vmcnt(11)
	v_mov_b64_e32 v[2:3], v[230:231]
	v_mov_b64_e32 v[4:5], v[232:233]
	v_lshlrev_b32_e32 v9, 16, v2
	v_mul_f32_e32 v9, 0xbfb8aa3b, v9
	v_exp_f32_e32 v9, v9
	v_and_b32_e32 v2, 0xffff0000, v2
	v_mul_f32_e32 v2, 0xbfb8aa3b, v2
	v_exp_f32_e32 v2, v2
	v_add_f32_e32 v9, 1.0, v9
	v_add_f32_e32 v2, 1.0, v2
	v_lshlrev_b32_e32 v31, 16, v3
	v_mul_f32_e32 v31, 0xbfb8aa3b, v31
	v_rcp_f32_e32 v179, v9
	v_exp_f32_e32 v31, v31
	s_nop 0
	v_add_f32_e32 v31, 1.0, v31
	v_and_b32_e32 v3, 0xffff0000, v3
	v_mul_f32_e32 v3, 0xbfb8aa3b, v3
	v_rcp_f32_e32 v9, v2
	v_exp_f32_e32 v3, v3
	s_nop 0
	v_add_f32_e32 v3, 1.0, v3
	v_rcp_f32_e32 v75, v31
	v_lshlrev_b32_e32 v31, 16, v4
	v_mul_f32_e32 v31, 0xbfb8aa3b, v31
	v_exp_f32_e32 v31, v31
	s_nop 0
	v_add_f32_e32 v31, 1.0, v31
	v_and_b32_e32 v4, 0xffff0000, v4
	v_mul_f32_e32 v4, 0xbfb8aa3b, v4
	v_exp_f32_e32 v4, v4
	v_rcp_f32_e32 v74, v3
	v_add_f32_e32 v4, 1.0, v4
	v_rcp_f32_e32 v76, v31
	v_lshlrev_b32_e32 v31, 16, v5
	v_mul_f32_e32 v31, 0xbfb8aa3b, v31
	v_exp_f32_e32 v31, v31
	s_nop 0
	v_add_f32_e32 v30, 1.0, v31
	v_rcp_f32_e32 v77, v4
	v_and_b32_e32 v4, 0xffff0000, v5
	v_mul_f32_e32 v4, 0xbfb8aa3b, v4
	v_exp_f32_e32 v4, v4
	s_nop 0
	v_add_f32_e32 v4, 1.0, v4
	v_rcp_f32_e32 v78, v30
	v_mov_b32_e32 v33, v24
	v_rcp_f32_e32 v79, v4
	s_waitcnt vmcnt(10)
	v_mov_b64_e32 v[20:21], v[246:247]
	v_cvt_pk_f32_fp8_e32 v[2:3], v20
	v_cvt_pk_f32_fp8_sdwa v[4:5], v20 src0_sel:WORD_1
	v_cvt_pk_f32_fp8_e32 v[30:31], v21
	v_cvt_pk_f32_fp8_sdwa v[20:21], v21 src0_sel:WORD_1
	v_mov_b32_e32 v32, v2
	v_pk_mul_f32 v[32:33], v[32:33], v[178:179]
	v_mov_b32_e32 v24, v3
	v_mov_b32_e32 v179, v9
	v_pk_mul_f32 v[2:3], v[24:25], v[178:179]
	v_mov_b32_e32 v179, v75
	v_add_f32_e32 v9, v2, v3
	v_mov_b32_e32 v2, v4
	v_mov_b32_e32 v3, v22
	v_pk_mul_f32 v[2:3], v[2:3], v[178:179]
	v_mov_b32_e32 v22, v5
	v_mov_b32_e32 v179, v74
	v_add_f32_e32 v4, v2, v3
	v_pk_mul_f32 v[2:3], v[22:23], v[178:179]
	v_mov_b32_e32 v179, v76
	v_add_f32_e32 v5, v2, v3
	v_mov_b32_e32 v2, v30
	v_mov_b32_e32 v3, v28
	v_pk_mul_f32 v[2:3], v[2:3], v[178:179]
	v_mov_b32_e32 v28, v31
	v_mov_b32_e32 v179, v77
	v_add_f32_e32 v22, v2, v3
	v_pk_mul_f32 v[2:3], v[28:29], v[178:179]
	v_mov_b32_e32 v179, v78
	v_add_f32_e32 v23, v2, v3
	v_mov_b32_e32 v2, v20
	v_mov_b32_e32 v3, v26
	v_pk_mul_f32 v[2:3], v[2:3], v[178:179]
	v_mov_b32_e32 v26, v21
	v_mov_b32_e32 v179, v79
	v_add_f32_e32 v32, v32, v33
	v_add_f32_e32 v20, v2, v3
	v_pk_mul_f32 v[2:3], v[26:27], v[178:179]
	v_mul_f32_e32 v4, 0x41800000, v4
	v_add_f32_e32 v21, v2, v3
	v_mul_f32_e32 v2, 0x41800000, v32
	v_mul_f32_e32 v3, 0x41800000, v9
	v_med3_f32 v9, v2, s57, v207
	v_med3_f32 v3, v3, s57, v207
	v_mov_b32_e32 v2, v167
	v_cvt_pk_fp8_f32 v2, v9, v3
	v_mul_f32_e32 v3, 0x41800000, v5
	v_med3_f32 v4, v4, s57, v207
	v_med3_f32 v3, v3, s57, v207
	v_cvt_pk_fp8_f32 v2, v4, v3 op_sel:[0,0,1]
	v_mul_f32_e32 v3, 0x41800000, v22
	v_mul_f32_e32 v4, 0x41800000, v23
	v_med3_f32 v9, v3, s57, v207
	v_med3_f32 v4, v4, s57, v207
	v_mov_b32_e32 v3, v167
	v_cvt_pk_fp8_f32 v3, v9, v4
	v_mul_f32_e32 v5, 0x41800000, v20
	v_mul_f32_e32 v4, 0x41800000, v21
	v_med3_f32 v5, v5, s57, v207
	v_med3_f32 v4, v4, s57, v207
	v_cvt_pk_fp8_f32 v3, v5, v4 op_sel:[0,0,1]
	v_lshl_add_u64 v[4:5], s[20:21], 0, v[18:19]
	v_lshl_add_u64 v[18:19], v[4:5], 0, v[6:7]
	v_pk_mul_f32 v[24:25], v[66:67], s[28:29] op_sel_hi:[1,0]
	global_store_dwordx2 v[18:19], v[2:3], off
	s_nop 0
	v_pk_mul_f32 v[20:21], v[70:71], s[28:29] op_sel_hi:[1,0]
	v_pk_mul_f32 v[16:17], v[72:73], s[28:29] op_sel_hi:[1,0]
	v_pk_mul_f32 v[22:23], v[68:69], s[28:29] op_sel_hi:[1,0]
	s_waitcnt vmcnt(9)
	v_mov_b64_e32 v[2:3], v[234:235]
	v_mov_b64_e32 v[4:5], v[236:237]
	v_lshlrev_b32_e32 v9, 16, v2
	v_mul_f32_e32 v9, 0xbfb8aa3b, v9
	v_exp_f32_e32 v9, v9
	v_and_b32_e32 v2, 0xffff0000, v2
	v_mul_f32_e32 v2, 0xbfb8aa3b, v2
	v_exp_f32_e32 v2, v2
	v_add_f32_e32 v9, 1.0, v9
	v_add_f32_e32 v2, 1.0, v2
	v_lshlrev_b32_e32 v27, 16, v3
	v_mul_f32_e32 v27, 0xbfb8aa3b, v27
	v_rcp_f32_e32 v179, v9
	v_exp_f32_e32 v27, v27
	s_nop 0
	v_add_f32_e32 v27, 1.0, v27
	v_and_b32_e32 v3, 0xffff0000, v3
	v_mul_f32_e32 v3, 0xbfb8aa3b, v3
	v_rcp_f32_e32 v9, v2
	v_exp_f32_e32 v3, v3
	s_nop 0
	v_add_f32_e32 v3, 1.0, v3
	v_rcp_f32_e32 v31, v27
	v_lshlrev_b32_e32 v27, 16, v4
	v_mul_f32_e32 v27, 0xbfb8aa3b, v27
	v_exp_f32_e32 v27, v27
	s_nop 0
	v_add_f32_e32 v27, 1.0, v27
	v_and_b32_e32 v4, 0xffff0000, v4
	v_mul_f32_e32 v4, 0xbfb8aa3b, v4
	v_exp_f32_e32 v4, v4
	v_rcp_f32_e32 v30, v3
	v_add_f32_e32 v4, 1.0, v4
	v_rcp_f32_e32 v32, v27
	v_lshlrev_b32_e32 v27, 16, v5
	v_mul_f32_e32 v27, 0xbfb8aa3b, v27
	v_exp_f32_e32 v27, v27
	s_nop 0
	v_add_f32_e32 v26, 1.0, v27
	v_rcp_f32_e32 v33, v4
	v_and_b32_e32 v4, 0xffff0000, v5
	v_mul_f32_e32 v4, 0xbfb8aa3b, v4
	v_exp_f32_e32 v4, v4
	s_nop 0
	v_add_f32_e32 v4, 1.0, v4
	v_rcp_f32_e32 v66, v26
	v_mov_b32_e32 v29, v20
	v_rcp_f32_e32 v67, v4
	s_waitcnt vmcnt(8)
	v_mov_b64_e32 v[14:15], v[248:249]
	v_cvt_pk_f32_fp8_e32 v[2:3], v14
	v_cvt_pk_f32_fp8_sdwa v[4:5], v14 src0_sel:WORD_1
	v_cvt_pk_f32_fp8_e32 v[26:27], v15
	v_cvt_pk_f32_fp8_sdwa v[14:15], v15 src0_sel:WORD_1
	v_mov_b32_e32 v28, v2
	v_pk_mul_f32 v[28:29], v[28:29], v[178:179]
	v_mov_b32_e32 v20, v3
	v_mov_b32_e32 v179, v9
	v_pk_mul_f32 v[2:3], v[20:21], v[178:179]
	v_mov_b32_e32 v179, v31
	v_add_f32_e32 v9, v2, v3
	v_mov_b32_e32 v2, v4
	v_mov_b32_e32 v3, v16
	v_pk_mul_f32 v[2:3], v[2:3], v[178:179]
	v_mov_b32_e32 v16, v5
	v_mov_b32_e32 v179, v30
	v_add_f32_e32 v4, v2, v3
	v_pk_mul_f32 v[2:3], v[16:17], v[178:179]
	v_mov_b32_e32 v179, v32
	v_add_f32_e32 v5, v2, v3
	v_mov_b32_e32 v2, v26
	v_mov_b32_e32 v3, v24
	v_pk_mul_f32 v[2:3], v[2:3], v[178:179]
	v_mov_b32_e32 v24, v27
	v_mov_b32_e32 v179, v33
	v_add_f32_e32 v16, v2, v3
	v_pk_mul_f32 v[2:3], v[24:25], v[178:179]
	v_mov_b32_e32 v179, v66
	v_add_f32_e32 v17, v2, v3
	v_mov_b32_e32 v2, v14
	v_mov_b32_e32 v3, v22
	v_pk_mul_f32 v[2:3], v[2:3], v[178:179]
	v_mov_b32_e32 v22, v15
	v_mov_b32_e32 v179, v67
	v_add_f32_e32 v28, v28, v29
	v_add_f32_e32 v14, v2, v3
	v_pk_mul_f32 v[2:3], v[22:23], v[178:179]
	v_mul_f32_e32 v4, 0x41800000, v4
	v_add_f32_e32 v15, v2, v3
	v_mul_f32_e32 v2, 0x41800000, v28
	v_mul_f32_e32 v3, 0x41800000, v9
	v_med3_f32 v9, v2, s57, v207
	v_med3_f32 v3, v3, s57, v207
	v_mov_b32_e32 v2, v167
	v_cvt_pk_fp8_f32 v2, v9, v3
	v_mul_f32_e32 v3, 0x41800000, v5
	v_med3_f32 v4, v4, s57, v207
	v_med3_f32 v3, v3, s57, v207
	v_cvt_pk_fp8_f32 v2, v4, v3 op_sel:[0,0,1]
	v_mul_f32_e32 v3, 0x41800000, v16
	v_mul_f32_e32 v4, 0x41800000, v17
	v_med3_f32 v9, v3, s57, v207
	v_med3_f32 v4, v4, s57, v207
	v_mov_b32_e32 v3, v167
	v_cvt_pk_fp8_f32 v3, v9, v4
	v_mul_f32_e32 v5, 0x41800000, v14
	v_mul_f32_e32 v4, 0x41800000, v15
	v_med3_f32 v5, v5, s57, v207
	v_med3_f32 v4, v4, s57, v207
	v_cvt_pk_fp8_f32 v3, v5, v4 op_sel:[0,0,1]
	v_add_u32_e32 v16, 0xa0, v8
	v_ashrrev_i32_e32 v17, 31, v16
	v_pk_mul_f32 v[28:29], v[58:59], s[28:29] op_sel_hi:[1,0]
	global_store_dwordx2 v[18:19], v[2:3], off offset:128
	v_mad_i64_i32 v[2:3], s[0:1], v16, s56, v[10:11]
	v_lshl_add_u64 v[14:15], v[2:3], 0, v[12:13]
	v_lshlrev_b64 v[18:19], 11, v[16:17]
	v_lshl_add_u64 v[16:17], s[16:17], 0, v[18:19]
	v_lshl_add_u64 v[16:17], v[16:17], 0, v[6:7]
	v_pk_mul_f32 v[26:27], v[60:61], s[28:29] op_sel_hi:[1,0]
	v_pk_mul_f32 v[24:25], v[62:63], s[28:29] op_sel_hi:[1,0]
	v_pk_mul_f32 v[22:23], v[64:65], s[28:29] op_sel_hi:[1,0]
	s_waitcnt vmcnt(7)
	v_mov_b64_e32 v[2:3], v[214:215]
	v_mov_b64_e32 v[4:5], v[216:217]
	v_lshlrev_b32_e32 v9, 16, v2
	v_mul_f32_e32 v9, 0xbfb8aa3b, v9
	v_exp_f32_e32 v9, v9
	v_and_b32_e32 v2, 0xffff0000, v2
	v_mul_f32_e32 v2, 0xbfb8aa3b, v2
	v_exp_f32_e32 v2, v2
	v_add_f32_e32 v9, 1.0, v9
	v_add_f32_e32 v2, 1.0, v2
	v_lshlrev_b32_e32 v31, 16, v3
	v_mul_f32_e32 v31, 0xbfb8aa3b, v31
	v_rcp_f32_e32 v179, v9
	v_exp_f32_e32 v31, v31
	s_nop 0
	v_add_f32_e32 v31, 1.0, v31
	v_and_b32_e32 v3, 0xffff0000, v3
	v_mul_f32_e32 v3, 0xbfb8aa3b, v3
	v_rcp_f32_e32 v9, v2
	v_exp_f32_e32 v3, v3
	s_nop 0
	v_add_f32_e32 v3, 1.0, v3
	v_rcp_f32_e32 v59, v31
	v_lshlrev_b32_e32 v31, 16, v4
	v_mul_f32_e32 v31, 0xbfb8aa3b, v31
	v_exp_f32_e32 v31, v31
	s_nop 0
	v_add_f32_e32 v31, 1.0, v31
	v_and_b32_e32 v4, 0xffff0000, v4
	v_mul_f32_e32 v4, 0xbfb8aa3b, v4
	v_exp_f32_e32 v4, v4
	v_rcp_f32_e32 v58, v3
	v_add_f32_e32 v4, 1.0, v4
	v_rcp_f32_e32 v60, v31
	v_lshlrev_b32_e32 v31, 16, v5
	v_mul_f32_e32 v31, 0xbfb8aa3b, v31
	v_exp_f32_e32 v31, v31
	s_nop 0
	v_add_f32_e32 v30, 1.0, v31
	v_rcp_f32_e32 v61, v4
	v_and_b32_e32 v4, 0xffff0000, v5
	v_mul_f32_e32 v4, 0xbfb8aa3b, v4
	v_exp_f32_e32 v4, v4
	s_nop 0
	v_add_f32_e32 v4, 1.0, v4
	v_rcp_f32_e32 v62, v30
	v_mov_b32_e32 v33, v24
	v_rcp_f32_e32 v63, v4
	s_waitcnt vmcnt(6)
	v_mov_b64_e32 v[20:21], v[238:239]
	v_cvt_pk_f32_fp8_e32 v[2:3], v20
	v_cvt_pk_f32_fp8_sdwa v[4:5], v20 src0_sel:WORD_1
	v_cvt_pk_f32_fp8_e32 v[30:31], v21
	v_cvt_pk_f32_fp8_sdwa v[20:21], v21 src0_sel:WORD_1
	v_mov_b32_e32 v32, v2
	v_pk_mul_f32 v[32:33], v[32:33], v[178:179]
	v_mov_b32_e32 v24, v3
	v_mov_b32_e32 v179, v9
	v_pk_mul_f32 v[2:3], v[24:25], v[178:179]
	v_mov_b32_e32 v179, v59
	v_add_f32_e32 v9, v2, v3
	v_mov_b32_e32 v2, v4
	v_mov_b32_e32 v3, v22
	v_pk_mul_f32 v[2:3], v[2:3], v[178:179]
	v_mov_b32_e32 v22, v5
	v_mov_b32_e32 v179, v58
	v_add_f32_e32 v4, v2, v3
	v_pk_mul_f32 v[2:3], v[22:23], v[178:179]
	v_mov_b32_e32 v179, v60
	v_add_f32_e32 v5, v2, v3
	v_mov_b32_e32 v2, v30
	v_mov_b32_e32 v3, v28
	v_pk_mul_f32 v[2:3], v[2:3], v[178:179]
	v_mov_b32_e32 v28, v31
	v_mov_b32_e32 v179, v61
	v_add_f32_e32 v22, v2, v3
	v_pk_mul_f32 v[2:3], v[28:29], v[178:179]
	v_mov_b32_e32 v179, v62
	v_add_f32_e32 v23, v2, v3
	v_mov_b32_e32 v2, v20
	v_mov_b32_e32 v3, v26
	v_pk_mul_f32 v[2:3], v[2:3], v[178:179]
	v_mov_b32_e32 v26, v21
	v_mov_b32_e32 v179, v63
	v_add_f32_e32 v32, v32, v33
	v_add_f32_e32 v20, v2, v3
	v_pk_mul_f32 v[2:3], v[26:27], v[178:179]
	v_mul_f32_e32 v4, 0x41800000, v4
	v_add_f32_e32 v21, v2, v3
	v_mul_f32_e32 v2, 0x41800000, v32
	v_mul_f32_e32 v3, 0x41800000, v9
	v_med3_f32 v9, v2, s57, v207
	v_med3_f32 v3, v3, s57, v207
	v_mov_b32_e32 v2, v167
	v_cvt_pk_fp8_f32 v2, v9, v3
	v_mul_f32_e32 v3, 0x41800000, v5
	v_med3_f32 v4, v4, s57, v207
	v_med3_f32 v3, v3, s57, v207
	v_cvt_pk_fp8_f32 v2, v4, v3 op_sel:[0,0,1]
	v_mul_f32_e32 v3, 0x41800000, v22
	v_mul_f32_e32 v4, 0x41800000, v23
	v_med3_f32 v9, v3, s57, v207
	v_med3_f32 v4, v4, s57, v207
	v_mov_b32_e32 v3, v167
	v_cvt_pk_fp8_f32 v3, v9, v4
	v_mul_f32_e32 v5, 0x41800000, v20
	v_mul_f32_e32 v4, 0x41800000, v21
	v_med3_f32 v5, v5, s57, v207
	v_med3_f32 v4, v4, s57, v207
	v_cvt_pk_fp8_f32 v3, v5, v4 op_sel:[0,0,1]
	v_lshl_add_u64 v[4:5], s[20:21], 0, v[18:19]
	v_lshl_add_u64 v[18:19], v[4:5], 0, v[6:7]
	v_pk_mul_f32 v[24:25], v[50:51], s[28:29] op_sel_hi:[1,0]
	global_store_dwordx2 v[18:19], v[2:3], off
	s_nop 0
	v_pk_mul_f32 v[20:21], v[54:55], s[28:29] op_sel_hi:[1,0]
	v_pk_mul_f32 v[16:17], v[56:57], s[28:29] op_sel_hi:[1,0]
	v_pk_mul_f32 v[22:23], v[52:53], s[28:29] op_sel_hi:[1,0]
	s_waitcnt vmcnt(5)
	v_mov_b64_e32 v[2:3], v[218:219]
	v_mov_b64_e32 v[4:5], v[220:221]
	v_lshlrev_b32_e32 v9, 16, v2
	v_mul_f32_e32 v9, 0xbfb8aa3b, v9
	v_exp_f32_e32 v9, v9
	v_and_b32_e32 v2, 0xffff0000, v2
	v_mul_f32_e32 v2, 0xbfb8aa3b, v2
	v_exp_f32_e32 v2, v2
	v_add_f32_e32 v9, 1.0, v9
	v_add_f32_e32 v2, 1.0, v2
	v_lshlrev_b32_e32 v27, 16, v3
	v_mul_f32_e32 v27, 0xbfb8aa3b, v27
	v_rcp_f32_e32 v179, v9
	v_exp_f32_e32 v27, v27
	s_nop 0
	v_add_f32_e32 v27, 1.0, v27
	v_and_b32_e32 v3, 0xffff0000, v3
	v_mul_f32_e32 v3, 0xbfb8aa3b, v3
	v_rcp_f32_e32 v9, v2
	v_exp_f32_e32 v3, v3
	s_nop 0
	v_add_f32_e32 v3, 1.0, v3
	v_rcp_f32_e32 v31, v27
	v_lshlrev_b32_e32 v27, 16, v4
	v_mul_f32_e32 v27, 0xbfb8aa3b, v27
	v_exp_f32_e32 v27, v27
	s_nop 0
	v_add_f32_e32 v27, 1.0, v27
	v_and_b32_e32 v4, 0xffff0000, v4
	v_mul_f32_e32 v4, 0xbfb8aa3b, v4
	v_exp_f32_e32 v4, v4
	v_rcp_f32_e32 v30, v3
	v_add_f32_e32 v4, 1.0, v4
	v_rcp_f32_e32 v32, v27
	v_lshlrev_b32_e32 v27, 16, v5
	v_mul_f32_e32 v27, 0xbfb8aa3b, v27
	v_exp_f32_e32 v27, v27
	s_nop 0
	v_add_f32_e32 v26, 1.0, v27
	v_rcp_f32_e32 v33, v4
	v_and_b32_e32 v4, 0xffff0000, v5
	v_mul_f32_e32 v4, 0xbfb8aa3b, v4
	v_exp_f32_e32 v4, v4
	s_nop 0
	v_add_f32_e32 v4, 1.0, v4
	v_rcp_f32_e32 v50, v26
	v_mov_b32_e32 v29, v20
	v_rcp_f32_e32 v51, v4
	s_waitcnt vmcnt(4)
	v_mov_b64_e32 v[14:15], v[240:241]
	v_cvt_pk_f32_fp8_e32 v[2:3], v14
	v_cvt_pk_f32_fp8_sdwa v[4:5], v14 src0_sel:WORD_1
	v_cvt_pk_f32_fp8_e32 v[26:27], v15
	v_cvt_pk_f32_fp8_sdwa v[14:15], v15 src0_sel:WORD_1
	v_mov_b32_e32 v28, v2
	v_pk_mul_f32 v[28:29], v[28:29], v[178:179]
	v_mov_b32_e32 v20, v3
	v_mov_b32_e32 v179, v9
	v_pk_mul_f32 v[2:3], v[20:21], v[178:179]
	v_mov_b32_e32 v179, v31
	v_add_f32_e32 v9, v2, v3
	v_mov_b32_e32 v2, v4
	v_mov_b32_e32 v3, v16
	v_pk_mul_f32 v[2:3], v[2:3], v[178:179]
	v_mov_b32_e32 v16, v5
	v_mov_b32_e32 v179, v30
	v_add_f32_e32 v4, v2, v3
	v_pk_mul_f32 v[2:3], v[16:17], v[178:179]
	v_mov_b32_e32 v179, v32
	v_add_f32_e32 v5, v2, v3
	v_mov_b32_e32 v2, v26
	v_mov_b32_e32 v3, v24
	v_pk_mul_f32 v[2:3], v[2:3], v[178:179]
	v_mov_b32_e32 v24, v27
	v_mov_b32_e32 v179, v33
	v_add_f32_e32 v16, v2, v3
	v_pk_mul_f32 v[2:3], v[24:25], v[178:179]
	v_mov_b32_e32 v179, v50
	v_add_f32_e32 v17, v2, v3
	v_mov_b32_e32 v2, v14
	v_mov_b32_e32 v3, v22
	v_pk_mul_f32 v[2:3], v[2:3], v[178:179]
	v_mov_b32_e32 v22, v15
	v_mov_b32_e32 v179, v51
	v_add_f32_e32 v28, v28, v29
	v_add_f32_e32 v14, v2, v3
	v_pk_mul_f32 v[2:3], v[22:23], v[178:179]
	v_mul_f32_e32 v4, 0x41800000, v4
	v_add_f32_e32 v15, v2, v3
	v_mul_f32_e32 v2, 0x41800000, v28
	v_mul_f32_e32 v3, 0x41800000, v9
	v_med3_f32 v9, v2, s57, v207
	v_med3_f32 v3, v3, s57, v207
	v_mov_b32_e32 v2, v167
	v_cvt_pk_fp8_f32 v2, v9, v3
	v_mul_f32_e32 v3, 0x41800000, v5
	v_med3_f32 v4, v4, s57, v207
	v_med3_f32 v3, v3, s57, v207
	v_cvt_pk_fp8_f32 v2, v4, v3 op_sel:[0,0,1]
	v_mul_f32_e32 v3, 0x41800000, v16
	v_mul_f32_e32 v4, 0x41800000, v17
	v_med3_f32 v9, v3, s57, v207
	v_med3_f32 v4, v4, s57, v207
	v_mov_b32_e32 v3, v167
	v_cvt_pk_fp8_f32 v3, v9, v4
	v_mul_f32_e32 v5, 0x41800000, v14
	v_mul_f32_e32 v4, 0x41800000, v15
	v_med3_f32 v5, v5, s57, v207
	v_med3_f32 v4, v4, s57, v207
	v_cvt_pk_fp8_f32 v3, v5, v4 op_sel:[0,0,1]
	v_add_u32_e32 v14, 0xb0, v8
	v_ashrrev_i32_e32 v15, 31, v14
	v_pk_mul_f32 v[22:23], v[42:43], s[28:29] op_sel_hi:[1,0]
	global_store_dwordx2 v[18:19], v[2:3], off offset:128
	v_mad_i64_i32 v[2:3], s[0:1], v14, s56, v[10:11]
	v_lshl_add_u64 v[8:9], v[2:3], 0, v[12:13]
	v_lshlrev_b64 v[12:13], 11, v[14:15]
	v_lshl_add_u64 v[10:11], s[16:17], 0, v[12:13]
	v_lshl_add_u64 v[10:11], v[10:11], 0, v[6:7]
	v_pk_mul_f32 v[20:21], v[44:45], s[28:29] op_sel_hi:[1,0]
	s_waitcnt vmcnt(3)
	v_mov_b64_e32 v[2:3], v[222:223]
	v_mov_b64_e32 v[4:5], v[224:225]
	v_lshlrev_b32_e32 v16, 16, v2
	v_mul_f32_e32 v16, 0xbfb8aa3b, v16
	v_exp_f32_e32 v18, v16
	v_and_b32_e32 v2, 0xffff0000, v2
	v_mul_f32_e32 v2, 0xbfb8aa3b, v2
	v_exp_f32_e32 v2, v2
	v_add_f32_e32 v24, 1.0, v18
	v_add_f32_e32 v2, 1.0, v2
	v_pk_mul_f32 v[18:19], v[46:47], s[28:29] op_sel_hi:[1,0]
	v_pk_mul_f32 v[16:17], v[48:49], s[28:29] op_sel_hi:[1,0]
	v_lshlrev_b32_e32 v26, 16, v3
	v_mul_f32_e32 v26, 0xbfb8aa3b, v26
	v_rcp_f32_e32 v179, v24
	v_exp_f32_e32 v26, v26
	s_nop 0
	v_add_f32_e32 v26, 1.0, v26
	v_and_b32_e32 v3, 0xffff0000, v3
	v_mul_f32_e32 v3, 0xbfb8aa3b, v3
	v_exp_f32_e32 v3, v3
	v_rcp_f32_e32 v29, v2
	v_add_f32_e32 v3, 1.0, v3
	v_rcp_f32_e32 v28, v26
	v_lshlrev_b32_e32 v26, 16, v4
	v_mul_f32_e32 v26, 0xbfb8aa3b, v26
	v_exp_f32_e32 v26, v26
	s_nop 0
	v_add_f32_e32 v25, 1.0, v26
	v_and_b32_e32 v4, 0xffff0000, v4
	v_mul_f32_e32 v4, 0xbfb8aa3b, v4
	v_exp_f32_e32 v4, v4
	v_rcp_f32_e32 v31, v3
	v_add_f32_e32 v4, 1.0, v4
	v_rcp_f32_e32 v30, v25
	v_lshlrev_b32_e32 v25, 16, v5
	v_mul_f32_e32 v25, 0xbfb8aa3b, v25
	v_exp_f32_e32 v25, v25
	s_nop 0
	v_add_f32_e32 v24, 1.0, v25
	v_rcp_f32_e32 v32, v4
	v_and_b32_e32 v4, 0xffff0000, v5
	v_mul_f32_e32 v4, 0xbfb8aa3b, v4
	v_exp_f32_e32 v4, v4
	s_nop 0
	v_add_f32_e32 v4, 1.0, v4
	v_rcp_f32_e32 v33, v24
	v_mov_b32_e32 v27, v18
	v_rcp_f32_e32 v42, v4
	s_waitcnt vmcnt(2)
	v_mov_b64_e32 v[14:15], v[242:243]
	v_cvt_pk_f32_fp8_e32 v[2:3], v14
	v_cvt_pk_f32_fp8_sdwa v[4:5], v14 src0_sel:WORD_1
	v_cvt_pk_f32_fp8_e32 v[24:25], v15
	v_cvt_pk_f32_fp8_sdwa v[14:15], v15 src0_sel:WORD_1
	v_mov_b32_e32 v26, v2
	v_pk_mul_f32 v[26:27], v[26:27], v[178:179]
	v_mov_b32_e32 v18, v3
	v_mov_b32_e32 v179, v29
	v_pk_mul_f32 v[2:3], v[18:19], v[178:179]
	v_mov_b32_e32 v179, v28
	v_add_f32_e32 v18, v2, v3
	v_mov_b32_e32 v2, v4
	v_mov_b32_e32 v3, v16
	v_pk_mul_f32 v[2:3], v[2:3], v[178:179]
	v_mov_b32_e32 v16, v5
	v_mov_b32_e32 v179, v31
	v_add_f32_e32 v4, v2, v3
	v_pk_mul_f32 v[2:3], v[16:17], v[178:179]
	v_mov_b32_e32 v179, v30
	v_add_f32_e32 v5, v2, v3
	v_mov_b32_e32 v2, v24
	v_mov_b32_e32 v3, v22
	v_pk_mul_f32 v[2:3], v[2:3], v[178:179]
	v_mov_b32_e32 v22, v25
	v_mov_b32_e32 v179, v32
	v_add_f32_e32 v16, v2, v3
	v_pk_mul_f32 v[2:3], v[22:23], v[178:179]
	v_mov_b32_e32 v179, v33
	v_add_f32_e32 v17, v2, v3
	v_mov_b32_e32 v2, v14
	v_mov_b32_e32 v3, v20
	v_pk_mul_f32 v[2:3], v[2:3], v[178:179]
	v_mov_b32_e32 v20, v15
	v_mov_b32_e32 v179, v42
	v_add_f32_e32 v26, v26, v27
	v_add_f32_e32 v14, v2, v3
	v_pk_mul_f32 v[2:3], v[20:21], v[178:179]
	v_mul_f32_e32 v4, 0x41800000, v4
	v_add_f32_e32 v15, v2, v3
	v_mul_f32_e32 v2, 0x41800000, v26
	v_mul_f32_e32 v3, 0x41800000, v18
	v_med3_f32 v18, v2, s57, v207
	v_med3_f32 v3, v3, s57, v207
	v_mov_b32_e32 v2, v167
	v_cvt_pk_fp8_f32 v2, v18, v3
	v_mul_f32_e32 v3, 0x41800000, v5
	v_med3_f32 v4, v4, s57, v207
	v_med3_f32 v3, v3, s57, v207
	v_cvt_pk_fp8_f32 v2, v4, v3 op_sel:[0,0,1]
	v_mul_f32_e32 v3, 0x41800000, v16
	v_mul_f32_e32 v4, 0x41800000, v17
	v_mul_f32_e32 v5, 0x41800000, v14
	v_med3_f32 v14, v3, s57, v207
	v_med3_f32 v4, v4, s57, v207
	v_mov_b32_e32 v3, v167
	v_cvt_pk_fp8_f32 v3, v14, v4
	v_mul_f32_e32 v4, 0x41800000, v15
	v_med3_f32 v5, v5, s57, v207
	v_med3_f32 v4, v4, s57, v207
	v_cvt_pk_fp8_f32 v3, v5, v4 op_sel:[0,0,1]
	v_lshl_add_u64 v[4:5], s[20:21], 0, v[12:13]
	v_lshl_add_u64 v[6:7], v[4:5], 0, v[6:7]
	v_pk_mul_f32 v[16:17], v[34:35], s[28:29] op_sel_hi:[1,0]
	global_store_dwordx2 v[6:7], v[2:3], off
	s_nop 0
	v_pk_mul_f32 v[14:15], v[36:37], s[28:29] op_sel_hi:[1,0]
	s_waitcnt vmcnt(1)
	v_mov_b64_e32 v[2:3], v[226:227]
	v_mov_b64_e32 v[4:5], v[228:229]
	v_lshlrev_b32_e32 v10, 16, v2
	v_mul_f32_e32 v10, 0xbfb8aa3b, v10
	v_exp_f32_e32 v12, v10
	v_and_b32_e32 v2, 0xffff0000, v2
	v_mul_f32_e32 v2, 0xbfb8aa3b, v2
	v_exp_f32_e32 v2, v2
	v_add_f32_e32 v18, 1.0, v12
	v_add_f32_e32 v2, 1.0, v2
	v_pk_mul_f32 v[12:13], v[38:39], s[28:29] op_sel_hi:[1,0]
	v_pk_mul_f32 v[10:11], v[40:41], s[28:29] op_sel_hi:[1,0]
	v_lshlrev_b32_e32 v20, 16, v3
	v_mul_f32_e32 v20, 0xbfb8aa3b, v20
	v_rcp_f32_e32 v179, v18
	v_exp_f32_e32 v20, v20
	s_nop 0
	v_add_f32_e32 v20, 1.0, v20
	v_and_b32_e32 v3, 0xffff0000, v3
	v_mul_f32_e32 v3, 0xbfb8aa3b, v3
	v_exp_f32_e32 v3, v3
	v_rcp_f32_e32 v23, v2
	v_add_f32_e32 v3, 1.0, v3
	v_rcp_f32_e32 v22, v20
	v_lshlrev_b32_e32 v20, 16, v4
	v_mul_f32_e32 v20, 0xbfb8aa3b, v20
	v_exp_f32_e32 v20, v20
	s_nop 0
	v_add_f32_e32 v19, 1.0, v20
	v_and_b32_e32 v4, 0xffff0000, v4
	v_mul_f32_e32 v4, 0xbfb8aa3b, v4
	v_exp_f32_e32 v4, v4
	v_rcp_f32_e32 v25, v3
	v_add_f32_e32 v4, 1.0, v4
	v_rcp_f32_e32 v24, v19
	v_lshlrev_b32_e32 v19, 16, v5
	v_mul_f32_e32 v19, 0xbfb8aa3b, v19
	v_exp_f32_e32 v19, v19
	s_nop 0
	v_add_f32_e32 v18, 1.0, v19
	v_rcp_f32_e32 v26, v4
	v_and_b32_e32 v4, 0xffff0000, v5
	v_mul_f32_e32 v4, 0xbfb8aa3b, v4
	v_exp_f32_e32 v4, v4
	s_nop 0
	v_add_f32_e32 v4, 1.0, v4
	v_rcp_f32_e32 v27, v18
	v_mov_b32_e32 v21, v12
	v_rcp_f32_e32 v28, v4
	s_waitcnt vmcnt(0)
	v_mov_b64_e32 v[8:9], v[244:245]
	v_cvt_pk_f32_fp8_e32 v[2:3], v8
	v_cvt_pk_f32_fp8_sdwa v[4:5], v8 src0_sel:WORD_1
	v_cvt_pk_f32_fp8_e32 v[18:19], v9
	v_cvt_pk_f32_fp8_sdwa v[8:9], v9 src0_sel:WORD_1
	v_mov_b32_e32 v20, v2
	v_pk_mul_f32 v[20:21], v[20:21], v[178:179]
	v_mov_b32_e32 v12, v3
	v_mov_b32_e32 v179, v23
	v_pk_mul_f32 v[2:3], v[12:13], v[178:179]
	v_mov_b32_e32 v179, v22
	v_add_f32_e32 v12, v2, v3
	v_mov_b32_e32 v2, v4
	v_mov_b32_e32 v3, v10
	v_pk_mul_f32 v[2:3], v[2:3], v[178:179]
	v_mov_b32_e32 v10, v5
	v_mov_b32_e32 v179, v25
	v_add_f32_e32 v4, v2, v3
	v_pk_mul_f32 v[2:3], v[10:11], v[178:179]
	v_mov_b32_e32 v179, v24
	v_add_f32_e32 v5, v2, v3
	v_mov_b32_e32 v2, v18
	v_mov_b32_e32 v3, v16
	v_pk_mul_f32 v[2:3], v[2:3], v[178:179]
	v_mov_b32_e32 v16, v19
	v_mov_b32_e32 v179, v26
	v_add_f32_e32 v10, v2, v3
	v_pk_mul_f32 v[2:3], v[16:17], v[178:179]
	v_mov_b32_e32 v179, v27
	v_add_f32_e32 v11, v2, v3
	v_mov_b32_e32 v2, v8
	v_mov_b32_e32 v3, v14
	v_pk_mul_f32 v[2:3], v[2:3], v[178:179]
	v_mov_b32_e32 v14, v9
	v_mov_b32_e32 v179, v28
	v_add_f32_e32 v20, v20, v21
	v_add_f32_e32 v8, v2, v3
	v_pk_mul_f32 v[2:3], v[14:15], v[178:179]
	v_mul_f32_e32 v4, 0x41800000, v4
	v_add_f32_e32 v9, v2, v3
	v_mul_f32_e32 v2, 0x41800000, v20
	v_mul_f32_e32 v3, 0x41800000, v12
	v_med3_f32 v12, v2, s57, v207
	v_med3_f32 v3, v3, s57, v207
	v_mov_b32_e32 v2, v167
	v_cvt_pk_fp8_f32 v2, v12, v3
	v_mul_f32_e32 v3, 0x41800000, v5
	v_med3_f32 v4, v4, s57, v207
	v_med3_f32 v3, v3, s57, v207
	v_cvt_pk_fp8_f32 v2, v4, v3 op_sel:[0,0,1]
	v_mul_f32_e32 v3, 0x41800000, v10
	v_mul_f32_e32 v4, 0x41800000, v11
	v_mul_f32_e32 v5, 0x41800000, v8
	v_med3_f32 v8, v3, s57, v207
	v_med3_f32 v4, v4, s57, v207
	v_mov_b32_e32 v3, v167
	v_cvt_pk_fp8_f32 v3, v8, v4
	v_mul_f32_e32 v4, 0x41800000, v9
	v_med3_f32 v5, v5, s57, v207
	v_med3_f32 v4, v4, s57, v207
	v_cvt_pk_fp8_f32 v3, v5, v4 op_sel:[0,0,1]
	s_andn2_b64 vcc, exec, s[6:7]
	s_mov_b64 s[0:1], -1
	global_store_dwordx2 v[6:7], v[2:3], off offset:128
	s_cbranch_vccnz .LBB0_1050
	s_andn2_b64 vcc, exec, s[14:15]
	s_cbranch_vccnz .LBB0_1049
	s_barrier
	s_branch .LBB0_1049
